# speedup vs baseline: 1.0205x; 1.0019x over previous
.LBB3_35:
	s_andn2_b64 vcc, exec, s[2:3]
	s_cbranch_vccnz .LBB3_39
	s_waitcnt vmcnt(4)
	v_ashrrev_i32_e32 v81, 31, v80
	v_lshl_add_u64 v[2:3], v[80:81], 3, s[20:21]
	v_add_co_u32_e32 v2, vcc, 0x48000, v2
	s_movk_i32 s8, 0x620
	s_nop 0
	v_addc_co_u32_e32 v3, vcc, 0, v3, vcc
	global_load_dwordx2 v[82:83], v[2:3], off
	v_and_b32_e32 v2, 0x70, v7
	v_bitop3_b32 v2, v0, v2, 48 bitop3:0x6c
	s_waitcnt vmcnt(4)
	v_mad_u64_u32 v[64:65], s[6:7], v9, s8, v[2:3]
	v_lshrrev_b32_e32 v3, 4, v92
	v_bitop3_b32 v3, v3, v0, 4 bitop3:0x36
	v_lshlrev_b32_e32 v3, 4, v3
	v_and_b32_e32 v4, 0x70, v3
	s_waitcnt vmcnt(3)
	v_mad_u64_u32 v[66:67], s[6:7], v8, s8, v[4:5]
	s_waitcnt vmcnt(2)
	v_mad_u64_u32 v[68:69], s[6:7], v6, s8, v[2:3]
	s_waitcnt vmcnt(1)
	v_mad_u64_u32 v[70:71], s[6:7], v1, s8, v[4:5]
	v_lshrrev_b32_e32 v85, 5, v92
	v_bfe_u32 v2, v0, 1, 3
	s_mov_b64 s[6:7], 0x1800
	s_add_u32 s4, s20, 0x4000000
	v_bitop3_b32 v32, v85, v2, 2 bitop3:0x36
	v_bitop3_b32 v33, v85, v2, 4 bitop3:0x36
	v_bitop3_b32 v34, v85, v2, 6 bitop3:0x36
	v_lshl_add_u64 v[2:3], v[86:87], 0, s[6:7]
	s_addc_u32 s5, s21, 0
	s_lshl_b32 s2, s27, 12
	s_addk_i32 s2, 0x6000
	v_lshrrev_b32_e32 v1, 1, v0
	v_or_b32_e32 v81, s2, v84
	v_lshlrev_b32_e32 v0, 7, v0
	v_and_b32_e32 v8, 0xf80, v0
	v_lshlrev_b32_e32 v9, 4, v32
	v_bitop3_b32 v1, v85, v1, 7 bitop3:0x78
	v_or3_b32 v96, s2, v9, v8
	v_lshlrev_b32_e32 v9, 4, v33
	v_lshlrev_b32_e32 v1, 4, v1
	v_or3_b32 v97, s2, v9, v8
	v_lshlrev_b32_e32 v9, 4, v34
	v_or3_b32 v95, s2, v1, v8
	v_or3_b32 v94, s2, v9, v8
	v_add_u32_e32 v98, 0x103c0, v84
	global_load_dwordx4 v[116:119], v64, s[4:5] offset:0
	global_load_dwordx4 v[120:123], v66, s[4:5] offset:0
	global_load_dwordx4 v[124:127], v68, s[4:5] offset:0
	global_load_dwordx4 v[128:131], v70, s[4:5] offset:0
	global_load_dwordx4 v[132:135], v64, s[4:5] offset:128
	global_load_dwordx4 v[136:139], v66, s[4:5] offset:128
	global_load_dwordx4 v[140:143], v68, s[4:5] offset:128
	global_load_dwordx4 v[144:147], v70, s[4:5] offset:128
	global_load_dwordx4 v[148:151], v64, s[4:5] offset:256
	global_load_dwordx4 v[152:155], v66, s[4:5] offset:256
	global_load_dwordx4 v[156:159], v68, s[4:5] offset:256
	global_load_dwordx4 v[72:75], v70, s[4:5] offset:256
	s_add_u32 m0, s46, 0x0
	s_nop 0
	global_load_lds_dwordx4 v76, s[40:41]
	s_add_u32 m0, s47, 0x0
	s_nop 0
	global_load_lds_dwordx4 v77, s[42:43]
	s_add_u32 m0, s48, 0x0
	s_nop 0
	global_load_lds_dwordx4 v78, s[44:45]
	s_add_u32 m0, s46, 0x3000
	s_add_u32 s40, s40, 0x1800
	s_addc_u32 s41, s41, 0
	global_load_lds_dwordx4 v76, s[40:41]
	s_add_u32 m0, s47, 0x3000
	s_add_u32 s42, s42, 0x1800
	s_addc_u32 s43, s43, 0
	global_load_lds_dwordx4 v77, s[42:43]
	s_add_u32 m0, s48, 0x3000
	s_add_u32 s44, s44, 0x1800
	s_addc_u32 s45, s45, 0
	global_load_lds_dwordx4 v78, s[44:45]
	s_add_u32 m0, s46, 0xd3c0
	s_add_u32 s40, s40, 0x1800
	s_addc_u32 s41, s41, 0
	global_load_lds_dwordx4 v76, s[40:41]
	s_add_u32 m0, s47, 0xd3c0
	s_add_u32 s42, s42, 0x1800
	s_addc_u32 s43, s43, 0
	global_load_lds_dwordx4 v77, s[42:43]
	s_add_u32 m0, s48, 0xd3c0
	s_add_u32 s44, s44, 0x1800
	s_addc_u32 s45, s45, 0
	global_load_lds_dwordx4 v78, s[44:45]
	s_add_u32 m0, s46, 0x103c0
	s_add_u32 s40, s40, 0x1800
	s_addc_u32 s41, s41, 0
	global_load_lds_dwordx4 v76, s[40:41]
	s_add_u32 m0, s47, 0x103c0
	s_add_u32 s42, s42, 0x1800
	s_addc_u32 s43, s43, 0
	global_load_lds_dwordx4 v77, s[42:43]
	s_add_u32 m0, s48, 0x103c0
	s_add_u32 s44, s44, 0x1800
	s_addc_u32 s45, s45, 0
	global_load_lds_dwordx4 v78, s[44:45]
	s_waitcnt vmcnt(20)
	ds_write_b128 v81, v[116:119]
	ds_write_b128 v81, v[120:123] offset:1024
	ds_write_b128 v81, v[124:127] offset:2048
	ds_write_b128 v81, v[128:131] offset:3072
	ds_read_b128 v[52:55], v95
	ds_read_b128 v[56:59], v96
	ds_read_b128 v[60:63], v97
	ds_read_b128 v[0:3], v94
	global_load_dwordx4 v[116:119], v64, s[4:5] offset:384
	global_load_dwordx4 v[120:123], v66, s[4:5] offset:384
	global_load_dwordx4 v[124:127], v68, s[4:5] offset:384
	global_load_dwordx4 v[128:131], v70, s[4:5] offset:384
	s_waitcnt vmcnt(13)
	s_waitcnt lgkmcnt(0)
	s_barrier
	ds_read_b128 v[4:7], v84 offset:0
	ds_read_b128 v[8:11], v84 offset:1024
	ds_read_b128 v[12:15], v84 offset:2048
	ds_read_b128 v[16:19], v84 offset:3072
	ds_read_b128 v[20:23], v84 offset:4096
	ds_read_b128 v[24:27], v84 offset:5120
	ds_read_b128 v[28:31], v84 offset:6144
	ds_read_b128 v[32:35], v84 offset:7168
	ds_read_b128 v[36:39], v84 offset:8192
	ds_read_b128 v[40:43], v84 offset:9216
	ds_read_b128 v[44:47], v84 offset:10240
	ds_read_b128 v[48:51], v84 offset:11264
	s_waitcnt lgkmcnt(6)
	v_mfma_f32_32x32x16_f16 a[80:95], v[4:7], v[52:55], 0
	v_mfma_f32_32x32x16_f16 a[64:79], v[8:11], v[52:55], 0
	v_mfma_f32_32x32x16_f16 a[48:63], v[12:15], v[52:55], 0
	s_waitcnt vmcnt(10)
	s_waitcnt lgkmcnt(0)
	s_barrier
	ds_read_b128 v[4:7], v84 offset:12288
	ds_read_b128 v[8:11], v84 offset:13312
	ds_read_b128 v[12:15], v84 offset:14336
	s_nop 0
	v_mfma_f32_32x32x16_f16 a[32:47], v[16:19], v[52:55], 0
	ds_read_b128 v[16:19], v84 offset:15360
	v_mfma_f32_32x32x16_f16 a[16:31], v[20:23], v[52:55], 0
	ds_read_b128 v[20:23], v84 offset:16384
	v_mfma_f32_32x32x16_f16 a[0:15], v[24:27], v[52:55], 0
	ds_read_b128 v[24:27], v84 offset:17408
	v_mfma_f32_32x32x16_f16 a[80:95], v[28:31], v[56:59], a[80:95]
	s_add_u32 m0, s46, 0x0
	s_add_u32 s40, s40, 0x1800
	s_addc_u32 s41, s41, 0
	global_load_lds_dwordx4 v76, s[40:41]
	v_mfma_f32_32x32x16_f16 a[64:79], v[32:35], v[56:59], a[64:79]
	v_mfma_f32_32x32x16_f16 a[48:63], v[36:39], v[56:59], a[48:63]
	s_add_u32 m0, s47, 0x0
	s_add_u32 s42, s42, 0x1800
	s_addc_u32 s43, s43, 0
	global_load_lds_dwordx4 v77, s[42:43]
	v_mfma_f32_32x32x16_f16 a[32:47], v[40:43], v[56:59], a[32:47]
	v_mfma_f32_32x32x16_f16 a[16:31], v[44:47], v[56:59], a[16:31]
	s_add_u32 m0, s48, 0x0
	s_add_u32 s44, s44, 0x1800
	s_addc_u32 s45, s45, 0
	global_load_lds_dwordx4 v78, s[44:45]
	v_mfma_f32_32x32x16_f16 a[0:15], v[48:51], v[56:59], a[0:15]
	ds_read_b128 v[28:31], v84 offset:18432
	ds_read_b128 v[32:35], v84 offset:19456
	ds_read_b128 v[36:39], v84 offset:20480
	ds_read_b128 v[40:43], v84 offset:21504
	ds_read_b128 v[44:47], v84 offset:22528
	ds_read_b128 v[48:51], v84 offset:23552
	s_waitcnt lgkmcnt(6)
	s_nop 0
	v_mfma_f32_32x32x16_f16 a[80:95], v[4:7], v[60:63], a[80:95]
	s_waitcnt vmcnt(23)
	ds_write_b128 v81, v[132:135]
	ds_write_b128 v81, v[136:139] offset:1024
	ds_write_b128 v81, v[140:143] offset:2048
	ds_write_b128 v81, v[144:147] offset:3072
	s_nop 0
	v_mfma_f32_32x32x16_f16 a[64:79], v[8:11], v[60:63], a[64:79]
	ds_read_b128 v[100:103], v95
	ds_read_b128 v[104:107], v96
	ds_read_b128 v[108:111], v97
	ds_read_b128 v[112:115], v94
	v_mfma_f32_32x32x16_f16 a[48:63], v[12:15], v[60:63], a[48:63]
	global_load_dwordx4 v[132:135], v64, s[4:5] offset:512
	global_load_dwordx4 v[136:139], v66, s[4:5] offset:512
	global_load_dwordx4 v[140:143], v68, s[4:5] offset:512
	global_load_dwordx4 v[144:147], v70, s[4:5] offset:512
	s_waitcnt vmcnt(14)
	s_waitcnt lgkmcnt(8)
	s_barrier
	ds_read_b128 v[4:7], v84 offset:54208
	ds_read_b128 v[8:11], v84 offset:55232
	ds_read_b128 v[12:15], v84 offset:56256
	s_nop 0
	v_mfma_f32_32x32x16_f16 a[32:47], v[16:19], v[60:63], a[32:47]
	ds_read_b128 v[16:19], v84 offset:57280
	v_mfma_f32_32x32x16_f16 a[16:31], v[20:23], v[60:63], a[16:31]
	ds_read_b128 v[20:23], v84 offset:58304
	v_mfma_f32_32x32x16_f16 a[0:15], v[24:27], v[60:63], a[0:15]
	ds_read_b128 v[24:27], v84 offset:59328
	v_mfma_f32_32x32x16_f16 a[80:95], v[28:31], v[0:3], a[80:95]
	s_add_u32 m0, s46, 0x3000
	s_add_u32 s40, s40, 0x1800
	s_addc_u32 s41, s41, 0
	global_load_lds_dwordx4 v76, s[40:41]
	s_nop 0
	v_mfma_f32_32x32x16_f16 a[64:79], v[32:35], v[0:3], a[64:79]
	v_mfma_f32_32x32x16_f16 a[48:63], v[36:39], v[0:3], a[48:63]
	s_add_u32 m0, s47, 0x3000
	s_add_u32 s42, s42, 0x1800
	s_addc_u32 s43, s43, 0
	global_load_lds_dwordx4 v77, s[42:43]
	s_nop 0
	v_mfma_f32_32x32x16_f16 a[32:47], v[40:43], v[0:3], a[32:47]
	v_mfma_f32_32x32x16_f16 a[16:31], v[44:47], v[0:3], a[16:31]
	s_add_u32 m0, s48, 0x3000
	s_add_u32 s44, s44, 0x1800
	s_addc_u32 s45, s45, 0
	global_load_lds_dwordx4 v78, s[44:45]
	s_nop 0
	v_mfma_f32_32x32x16_f16 a[0:15], v[48:51], v[0:3], a[0:15]
	s_waitcnt lgkmcnt(6)
	ds_read_b128 v[28:31], v84 offset:60352
	ds_read_b128 v[32:35], v84 offset:61376
	ds_read_b128 v[36:39], v84 offset:62400
	ds_read_b128 v[40:43], v84 offset:63424
	ds_read_b128 v[44:47], v84 offset:64448
	ds_read_b128 v[48:51], v84 offset:65472
	s_waitcnt lgkmcnt(6)
	v_mfma_f32_32x32x16_f16 a[80:95], v[4:7], v[100:103], a[80:95]
	v_mfma_f32_32x32x16_f16 a[64:79], v[8:11], v[100:103], a[64:79]
	v_mfma_f32_32x32x16_f16 a[48:63], v[12:15], v[100:103], a[48:63]
	s_waitcnt vmcnt(14)
	s_waitcnt lgkmcnt(0)
	s_barrier
	ds_read_b128 v[4:7], v98
	ds_read_b128 v[8:11], v98 offset:1024
	ds_read_b128 v[12:15], v98 offset:2048
	s_nop 0
	v_mfma_f32_32x32x16_f16 a[32:47], v[16:19], v[100:103], a[32:47]
	ds_read_b128 v[16:19], v98 offset:3072
	v_mfma_f32_32x32x16_f16 a[16:31], v[20:23], v[100:103], a[16:31]
	ds_read_b128 v[20:23], v98 offset:4096
	v_mfma_f32_32x32x16_f16 a[0:15], v[24:27], v[100:103], a[0:15]
	ds_read_b128 v[24:27], v98 offset:5120
	v_mfma_f32_32x32x16_f16 a[80:95], v[28:31], v[104:107], a[80:95]
	s_add_u32 m0, s46, 0xd3c0
	s_add_u32 s40, s40, 0x1800
	s_addc_u32 s41, s41, 0
	global_load_lds_dwordx4 v76, s[40:41]
	s_nop 0
	v_mfma_f32_32x32x16_f16 a[64:79], v[32:35], v[104:107], a[64:79]
	v_mfma_f32_32x32x16_f16 a[48:63], v[36:39], v[104:107], a[48:63]
	s_add_u32 m0, s47, 0xd3c0
	s_add_u32 s42, s42, 0x1800
	s_addc_u32 s43, s43, 0
	global_load_lds_dwordx4 v77, s[42:43]
	s_nop 0
	v_mfma_f32_32x32x16_f16 a[32:47], v[40:43], v[104:107], a[32:47]
	v_mfma_f32_32x32x16_f16 a[16:31], v[44:47], v[104:107], a[16:31]
	s_add_u32 m0, s48, 0xd3c0
	s_add_u32 s44, s44, 0x1800
	s_addc_u32 s45, s45, 0
	global_load_lds_dwordx4 v78, s[44:45]
	s_nop 0
	v_mfma_f32_32x32x16_f16 a[0:15], v[48:51], v[104:107], a[0:15]
	ds_read_b128 v[28:31], v98 offset:6144
	ds_read_b128 v[32:35], v98 offset:7168
	ds_read_b128 v[36:39], v98 offset:8192
	ds_read_b128 v[40:43], v98 offset:9216
	ds_read_b128 v[44:47], v98 offset:10240
	ds_read_b128 v[48:51], v98 offset:11264
	s_waitcnt lgkmcnt(6)
	s_nop 0
	v_mfma_f32_32x32x16_f16 a[80:95], v[4:7], v[108:111], a[80:95]
	s_waitcnt vmcnt(29)
	ds_write_b128 v81, v[148:151]
	ds_write_b128 v81, v[152:155] offset:1024
	ds_write_b128 v81, v[156:159] offset:2048
	ds_write_b128 v81, v[72:75] offset:3072
	s_nop 0
	v_mfma_f32_32x32x16_f16 a[64:79], v[8:11], v[108:111], a[64:79]
	ds_read_b128 v[52:55], v95
	ds_read_b128 v[56:59], v96
	ds_read_b128 v[60:63], v97
	ds_read_b128 v[0:3], v94
	v_mfma_f32_32x32x16_f16 a[48:63], v[12:15], v[108:111], a[48:63]
	global_load_dwordx4 v[148:151], v64, s[4:5] offset:640
	global_load_dwordx4 v[152:155], v66, s[4:5] offset:640
	global_load_dwordx4 v[156:159], v68, s[4:5] offset:640
	global_load_dwordx4 v[72:75], v70, s[4:5] offset:640
	s_waitcnt vmcnt(14)
	s_waitcnt lgkmcnt(8)
	s_barrier
	ds_read_b128 v[4:7], v84 offset:0
	ds_read_b128 v[8:11], v84 offset:1024
	ds_read_b128 v[12:15], v84 offset:2048
	s_nop 0
	v_mfma_f32_32x32x16_f16 a[32:47], v[16:19], v[108:111], a[32:47]
	ds_read_b128 v[16:19], v84 offset:3072
	v_mfma_f32_32x32x16_f16 a[16:31], v[20:23], v[108:111], a[16:31]
	ds_read_b128 v[20:23], v84 offset:4096
	v_mfma_f32_32x32x16_f16 a[0:15], v[24:27], v[108:111], a[0:15]
	ds_read_b128 v[24:27], v84 offset:5120
	v_mfma_f32_32x32x16_f16 a[80:95], v[28:31], v[112:115], a[80:95]
	s_add_u32 m0, s46, 0x103c0
	s_add_u32 s40, s40, 0x1800
	s_addc_u32 s41, s41, 0
	global_load_lds_dwordx4 v76, s[40:41]
	s_nop 0
	v_mfma_f32_32x32x16_f16 a[64:79], v[32:35], v[112:115], a[64:79]
	v_mfma_f32_32x32x16_f16 a[48:63], v[36:39], v[112:115], a[48:63]
	s_add_u32 m0, s47, 0x103c0
	s_add_u32 s42, s42, 0x1800
	s_addc_u32 s43, s43, 0
	global_load_lds_dwordx4 v77, s[42:43]
	s_nop 0
	v_mfma_f32_32x32x16_f16 a[32:47], v[40:43], v[112:115], a[32:47]
	v_mfma_f32_32x32x16_f16 a[16:31], v[44:47], v[112:115], a[16:31]
	s_add_u32 m0, s48, 0x103c0
	s_add_u32 s44, s44, 0x1800
	s_addc_u32 s45, s45, 0
	global_load_lds_dwordx4 v78, s[44:45]
	s_nop 0
	v_mfma_f32_32x32x16_f16 a[0:15], v[48:51], v[112:115], a[0:15]
	s_waitcnt lgkmcnt(6)
	ds_read_b128 v[28:31], v84 offset:6144
	ds_read_b128 v[32:35], v84 offset:7168
	ds_read_b128 v[36:39], v84 offset:8192
	ds_read_b128 v[40:43], v84 offset:9216
	ds_read_b128 v[44:47], v84 offset:10240
	ds_read_b128 v[48:51], v84 offset:11264
	s_waitcnt lgkmcnt(6)
	v_mfma_f32_32x32x16_f16 a[80:95], v[4:7], v[52:55], a[80:95]
	v_mfma_f32_32x32x16_f16 a[64:79], v[8:11], v[52:55], a[64:79]
	v_mfma_f32_32x32x16_f16 a[48:63], v[12:15], v[52:55], a[48:63]
	s_waitcnt vmcnt(10)
	s_waitcnt lgkmcnt(0)
	s_barrier
	ds_read_b128 v[4:7], v84 offset:12288
	ds_read_b128 v[8:11], v84 offset:13312
	ds_read_b128 v[12:15], v84 offset:14336
	s_nop 0
	v_mfma_f32_32x32x16_f16 a[32:47], v[16:19], v[52:55], a[32:47]
	ds_read_b128 v[16:19], v84 offset:15360
	v_mfma_f32_32x32x16_f16 a[16:31], v[20:23], v[52:55], a[16:31]
	ds_read_b128 v[20:23], v84 offset:16384
	v_mfma_f32_32x32x16_f16 a[0:15], v[24:27], v[52:55], a[0:15]
	ds_read_b128 v[24:27], v84 offset:17408
	v_mfma_f32_32x32x16_f16 a[80:95], v[28:31], v[56:59], a[80:95]
	s_add_u32 m0, s46, 0x0
	s_add_u32 s40, s40, 0x1800
	s_addc_u32 s41, s41, 0
	global_load_lds_dwordx4 v76, s[40:41]
	v_mfma_f32_32x32x16_f16 a[64:79], v[32:35], v[56:59], a[64:79]
	v_mfma_f32_32x32x16_f16 a[48:63], v[36:39], v[56:59], a[48:63]
	s_add_u32 m0, s47, 0x0
	s_add_u32 s42, s42, 0x1800
	s_addc_u32 s43, s43, 0
	global_load_lds_dwordx4 v77, s[42:43]
	v_mfma_f32_32x32x16_f16 a[32:47], v[40:43], v[56:59], a[32:47]
	v_mfma_f32_32x32x16_f16 a[16:31], v[44:47], v[56:59], a[16:31]
	s_add_u32 m0, s48, 0x0
	s_add_u32 s44, s44, 0x1800
	s_addc_u32 s45, s45, 0
	global_load_lds_dwordx4 v78, s[44:45]
	v_mfma_f32_32x32x16_f16 a[0:15], v[48:51], v[56:59], a[0:15]
	ds_read_b128 v[28:31], v84 offset:18432
	ds_read_b128 v[32:35], v84 offset:19456
	ds_read_b128 v[36:39], v84 offset:20480
	ds_read_b128 v[40:43], v84 offset:21504
	ds_read_b128 v[44:47], v84 offset:22528
	ds_read_b128 v[48:51], v84 offset:23552
	s_waitcnt lgkmcnt(6)
	s_nop 0
	v_mfma_f32_32x32x16_f16 a[80:95], v[4:7], v[60:63], a[80:95]
	s_waitcnt vmcnt(23)
	ds_write_b128 v81, v[116:119]
	ds_write_b128 v81, v[120:123] offset:1024
	ds_write_b128 v81, v[124:127] offset:2048
	ds_write_b128 v81, v[128:131] offset:3072
	s_nop 0
	v_mfma_f32_32x32x16_f16 a[64:79], v[8:11], v[60:63], a[64:79]
	ds_read_b128 v[100:103], v95
	ds_read_b128 v[104:107], v96
	ds_read_b128 v[108:111], v97
	ds_read_b128 v[112:115], v94
	v_mfma_f32_32x32x16_f16 a[48:63], v[12:15], v[60:63], a[48:63]
	global_load_dwordx4 v[116:119], v64, s[4:5] offset:768
	global_load_dwordx4 v[120:123], v66, s[4:5] offset:768
	global_load_dwordx4 v[124:127], v68, s[4:5] offset:768
	global_load_dwordx4 v[128:131], v70, s[4:5] offset:768
	s_waitcnt vmcnt(14)
	s_waitcnt lgkmcnt(8)
	s_barrier
	ds_read_b128 v[4:7], v84 offset:54208
	ds_read_b128 v[8:11], v84 offset:55232
	ds_read_b128 v[12:15], v84 offset:56256
	s_nop 0
	v_mfma_f32_32x32x16_f16 a[32:47], v[16:19], v[60:63], a[32:47]
	ds_read_b128 v[16:19], v84 offset:57280
	v_mfma_f32_32x32x16_f16 a[16:31], v[20:23], v[60:63], a[16:31]
	ds_read_b128 v[20:23], v84 offset:58304
	v_mfma_f32_32x32x16_f16 a[0:15], v[24:27], v[60:63], a[0:15]
	ds_read_b128 v[24:27], v84 offset:59328
	v_mfma_f32_32x32x16_f16 a[80:95], v[28:31], v[0:3], a[80:95]
	s_add_u32 m0, s46, 0x3000
	s_add_u32 s40, s40, 0x1800
	s_addc_u32 s41, s41, 0
	global_load_lds_dwordx4 v76, s[40:41]
	s_nop 0
	v_mfma_f32_32x32x16_f16 a[64:79], v[32:35], v[0:3], a[64:79]
	v_mfma_f32_32x32x16_f16 a[48:63], v[36:39], v[0:3], a[48:63]
	s_add_u32 m0, s47, 0x3000
	s_add_u32 s42, s42, 0x1800
	s_addc_u32 s43, s43, 0
	global_load_lds_dwordx4 v77, s[42:43]
	s_nop 0
	v_mfma_f32_32x32x16_f16 a[32:47], v[40:43], v[0:3], a[32:47]
	v_mfma_f32_32x32x16_f16 a[16:31], v[44:47], v[0:3], a[16:31]
	s_add_u32 m0, s48, 0x3000
	s_add_u32 s44, s44, 0x1800
	s_addc_u32 s45, s45, 0
	global_load_lds_dwordx4 v78, s[44:45]
	s_nop 0
	v_mfma_f32_32x32x16_f16 a[0:15], v[48:51], v[0:3], a[0:15]
	s_waitcnt lgkmcnt(6)
	ds_read_b128 v[28:31], v84 offset:60352
	ds_read_b128 v[32:35], v84 offset:61376
	ds_read_b128 v[36:39], v84 offset:62400
	ds_read_b128 v[40:43], v84 offset:63424
	ds_read_b128 v[44:47], v84 offset:64448
	ds_read_b128 v[48:51], v84 offset:65472
	s_waitcnt lgkmcnt(6)
	v_mfma_f32_32x32x16_f16 a[80:95], v[4:7], v[100:103], a[80:95]
	v_mfma_f32_32x32x16_f16 a[64:79], v[8:11], v[100:103], a[64:79]
	v_mfma_f32_32x32x16_f16 a[48:63], v[12:15], v[100:103], a[48:63]
	s_waitcnt vmcnt(10)
	s_waitcnt lgkmcnt(0)
	s_barrier
	ds_read_b128 v[4:7], v98
	ds_read_b128 v[8:11], v98 offset:1024
	ds_read_b128 v[12:15], v98 offset:2048
	s_nop 0
	v_mfma_f32_32x32x16_f16 a[32:47], v[16:19], v[100:103], a[32:47]
	ds_read_b128 v[16:19], v98 offset:3072
	v_mfma_f32_32x32x16_f16 a[16:31], v[20:23], v[100:103], a[16:31]
	ds_read_b128 v[20:23], v98 offset:4096
	v_mfma_f32_32x32x16_f16 a[0:15], v[24:27], v[100:103], a[0:15]
	ds_read_b128 v[24:27], v98 offset:5120
	v_mfma_f32_32x32x16_f16 a[80:95], v[28:31], v[104:107], a[80:95]
	s_add_u32 m0, s46, 0xd3c0
	s_add_u32 s40, s40, 0x1800
	s_addc_u32 s41, s41, 0
	global_load_lds_dwordx4 v76, s[40:41]
	s_nop 0
	v_mfma_f32_32x32x16_f16 a[64:79], v[32:35], v[104:107], a[64:79]
	v_mfma_f32_32x32x16_f16 a[48:63], v[36:39], v[104:107], a[48:63]
	s_add_u32 m0, s47, 0xd3c0
	s_add_u32 s42, s42, 0x1800
	s_addc_u32 s43, s43, 0
	global_load_lds_dwordx4 v77, s[42:43]
	s_nop 0
	v_mfma_f32_32x32x16_f16 a[32:47], v[40:43], v[104:107], a[32:47]
	v_mfma_f32_32x32x16_f16 a[16:31], v[44:47], v[104:107], a[16:31]
	s_add_u32 m0, s48, 0xd3c0
	s_add_u32 s44, s44, 0x1800
	s_addc_u32 s45, s45, 0
	global_load_lds_dwordx4 v78, s[44:45]
	s_nop 0
	v_mfma_f32_32x32x16_f16 a[0:15], v[48:51], v[104:107], a[0:15]
	ds_read_b128 v[28:31], v98 offset:6144
	ds_read_b128 v[32:35], v98 offset:7168
	ds_read_b128 v[36:39], v98 offset:8192
	ds_read_b128 v[40:43], v98 offset:9216
	ds_read_b128 v[44:47], v98 offset:10240
	ds_read_b128 v[48:51], v98 offset:11264
	s_waitcnt lgkmcnt(6)
	s_nop 0
	v_mfma_f32_32x32x16_f16 a[80:95], v[4:7], v[108:111], a[80:95]
	s_waitcnt vmcnt(26)
	ds_write_b128 v81, v[132:135]
	ds_write_b128 v81, v[136:139] offset:1024
	ds_write_b128 v81, v[140:143] offset:2048
	ds_write_b128 v81, v[144:147] offset:3072
	s_nop 0
	v_mfma_f32_32x32x16_f16 a[64:79], v[8:11], v[108:111], a[64:79]
	ds_read_b128 v[52:55], v95
	ds_read_b128 v[56:59], v96
	ds_read_b128 v[60:63], v97
	ds_read_b128 v[0:3], v94
	v_mfma_f32_32x32x16_f16 a[48:63], v[12:15], v[108:111], a[48:63]
	global_load_dwordx4 v[132:135], v64, s[4:5] offset:896
	global_load_dwordx4 v[136:139], v66, s[4:5] offset:896
	global_load_dwordx4 v[140:143], v68, s[4:5] offset:896
	global_load_dwordx4 v[144:147], v70, s[4:5] offset:896
	s_waitcnt vmcnt(14)
	s_waitcnt lgkmcnt(8)
	s_barrier
	ds_read_b128 v[4:7], v84 offset:0
	ds_read_b128 v[8:11], v84 offset:1024
	ds_read_b128 v[12:15], v84 offset:2048
	s_nop 0
	v_mfma_f32_32x32x16_f16 a[32:47], v[16:19], v[108:111], a[32:47]
	ds_read_b128 v[16:19], v84 offset:3072
	v_mfma_f32_32x32x16_f16 a[16:31], v[20:23], v[108:111], a[16:31]
	ds_read_b128 v[20:23], v84 offset:4096
	v_mfma_f32_32x32x16_f16 a[0:15], v[24:27], v[108:111], a[0:15]
	ds_read_b128 v[24:27], v84 offset:5120
	v_mfma_f32_32x32x16_f16 a[80:95], v[28:31], v[112:115], a[80:95]
	s_add_u32 m0, s46, 0x103c0
	s_add_u32 s40, s40, 0x1800
	s_addc_u32 s41, s41, 0
	global_load_lds_dwordx4 v76, s[40:41]
	s_nop 0
	v_mfma_f32_32x32x16_f16 a[64:79], v[32:35], v[112:115], a[64:79]
	v_mfma_f32_32x32x16_f16 a[48:63], v[36:39], v[112:115], a[48:63]
	s_add_u32 m0, s47, 0x103c0
	s_add_u32 s42, s42, 0x1800
	s_addc_u32 s43, s43, 0
	global_load_lds_dwordx4 v77, s[42:43]
	s_nop 0
	v_mfma_f32_32x32x16_f16 a[32:47], v[40:43], v[112:115], a[32:47]
	v_mfma_f32_32x32x16_f16 a[16:31], v[44:47], v[112:115], a[16:31]
	s_add_u32 m0, s48, 0x103c0
	s_add_u32 s44, s44, 0x1800
	s_addc_u32 s45, s45, 0
	global_load_lds_dwordx4 v78, s[44:45]
	s_nop 0
	v_mfma_f32_32x32x16_f16 a[0:15], v[48:51], v[112:115], a[0:15]
	s_waitcnt lgkmcnt(6)
	ds_read_b128 v[28:31], v84 offset:6144
	ds_read_b128 v[32:35], v84 offset:7168
	ds_read_b128 v[36:39], v84 offset:8192
	ds_read_b128 v[40:43], v84 offset:9216
	ds_read_b128 v[44:47], v84 offset:10240
	ds_read_b128 v[48:51], v84 offset:11264
	s_waitcnt lgkmcnt(6)
	v_mfma_f32_32x32x16_f16 a[80:95], v[4:7], v[52:55], a[80:95]
	v_mfma_f32_32x32x16_f16 a[64:79], v[8:11], v[52:55], a[64:79]
	v_mfma_f32_32x32x16_f16 a[48:63], v[12:15], v[52:55], a[48:63]
	s_waitcnt vmcnt(10)
	s_waitcnt lgkmcnt(0)
	s_barrier
	ds_read_b128 v[4:7], v84 offset:12288
	ds_read_b128 v[8:11], v84 offset:13312
	ds_read_b128 v[12:15], v84 offset:14336
	s_nop 0
	v_mfma_f32_32x32x16_f16 a[32:47], v[16:19], v[52:55], a[32:47]
	ds_read_b128 v[16:19], v84 offset:15360
	v_mfma_f32_32x32x16_f16 a[16:31], v[20:23], v[52:55], a[16:31]
	ds_read_b128 v[20:23], v84 offset:16384
	v_mfma_f32_32x32x16_f16 a[0:15], v[24:27], v[52:55], a[0:15]
	ds_read_b128 v[24:27], v84 offset:17408
	v_mfma_f32_32x32x16_f16 a[80:95], v[28:31], v[56:59], a[80:95]
	s_add_u32 m0, s46, 0x0
	s_add_u32 s40, s40, 0x1800
	s_addc_u32 s41, s41, 0
	global_load_lds_dwordx4 v76, s[40:41]
	v_mfma_f32_32x32x16_f16 a[64:79], v[32:35], v[56:59], a[64:79]
	v_mfma_f32_32x32x16_f16 a[48:63], v[36:39], v[56:59], a[48:63]
	s_add_u32 m0, s47, 0x0
	s_add_u32 s42, s42, 0x1800
	s_addc_u32 s43, s43, 0
	global_load_lds_dwordx4 v77, s[42:43]
	v_mfma_f32_32x32x16_f16 a[32:47], v[40:43], v[56:59], a[32:47]
	v_mfma_f32_32x32x16_f16 a[16:31], v[44:47], v[56:59], a[16:31]
	s_add_u32 m0, s48, 0x0
	s_add_u32 s44, s44, 0x1800
	s_addc_u32 s45, s45, 0
	global_load_lds_dwordx4 v78, s[44:45]
	v_mfma_f32_32x32x16_f16 a[0:15], v[48:51], v[56:59], a[0:15]
	ds_read_b128 v[28:31], v84 offset:18432
	ds_read_b128 v[32:35], v84 offset:19456
	ds_read_b128 v[36:39], v84 offset:20480
	ds_read_b128 v[40:43], v84 offset:21504
	ds_read_b128 v[44:47], v84 offset:22528
	ds_read_b128 v[48:51], v84 offset:23552
	s_waitcnt lgkmcnt(6)
	s_nop 0
	v_mfma_f32_32x32x16_f16 a[80:95], v[4:7], v[60:63], a[80:95]
	s_waitcnt vmcnt(26)
	ds_write_b128 v81, v[148:151]
	ds_write_b128 v81, v[152:155] offset:1024
	ds_write_b128 v81, v[156:159] offset:2048
	ds_write_b128 v81, v[72:75] offset:3072
	s_nop 0
	v_mfma_f32_32x32x16_f16 a[64:79], v[8:11], v[60:63], a[64:79]
	ds_read_b128 v[100:103], v95
	ds_read_b128 v[104:107], v96
	ds_read_b128 v[108:111], v97
	ds_read_b128 v[112:115], v94
	v_mfma_f32_32x32x16_f16 a[48:63], v[12:15], v[60:63], a[48:63]
	global_load_dwordx4 v[148:151], v64, s[4:5] offset:1024
	global_load_dwordx4 v[152:155], v66, s[4:5] offset:1024
	global_load_dwordx4 v[156:159], v68, s[4:5] offset:1024
	global_load_dwordx4 v[72:75], v70, s[4:5] offset:1024
	s_waitcnt vmcnt(14)
	s_waitcnt lgkmcnt(8)
	s_barrier
	ds_read_b128 v[4:7], v84 offset:54208
	ds_read_b128 v[8:11], v84 offset:55232
	ds_read_b128 v[12:15], v84 offset:56256
	s_nop 0
	v_mfma_f32_32x32x16_f16 a[32:47], v[16:19], v[60:63], a[32:47]
	ds_read_b128 v[16:19], v84 offset:57280
	v_mfma_f32_32x32x16_f16 a[16:31], v[20:23], v[60:63], a[16:31]
	ds_read_b128 v[20:23], v84 offset:58304
	v_mfma_f32_32x32x16_f16 a[0:15], v[24:27], v[60:63], a[0:15]
	ds_read_b128 v[24:27], v84 offset:59328
	v_mfma_f32_32x32x16_f16 a[80:95], v[28:31], v[0:3], a[80:95]
	s_add_u32 m0, s46, 0x3000
	s_add_u32 s40, s40, 0x1800
	s_addc_u32 s41, s41, 0
	global_load_lds_dwordx4 v76, s[40:41]
	s_nop 0
	v_mfma_f32_32x32x16_f16 a[64:79], v[32:35], v[0:3], a[64:79]
	v_mfma_f32_32x32x16_f16 a[48:63], v[36:39], v[0:3], a[48:63]
	s_add_u32 m0, s47, 0x3000
	s_add_u32 s42, s42, 0x1800
	s_addc_u32 s43, s43, 0
	global_load_lds_dwordx4 v77, s[42:43]
	s_nop 0
	v_mfma_f32_32x32x16_f16 a[32:47], v[40:43], v[0:3], a[32:47]
	v_mfma_f32_32x32x16_f16 a[16:31], v[44:47], v[0:3], a[16:31]
	s_add_u32 m0, s48, 0x3000
	s_add_u32 s44, s44, 0x1800
	s_addc_u32 s45, s45, 0
	global_load_lds_dwordx4 v78, s[44:45]
	s_nop 0
	v_mfma_f32_32x32x16_f16 a[0:15], v[48:51], v[0:3], a[0:15]
	s_waitcnt lgkmcnt(6)
	ds_read_b128 v[28:31], v84 offset:60352
	ds_read_b128 v[32:35], v84 offset:61376
	ds_read_b128 v[36:39], v84 offset:62400
	ds_read_b128 v[40:43], v84 offset:63424
	ds_read_b128 v[44:47], v84 offset:64448
	ds_read_b128 v[48:51], v84 offset:65472
	s_waitcnt lgkmcnt(6)
	v_mfma_f32_32x32x16_f16 a[80:95], v[4:7], v[100:103], a[80:95]
	v_mfma_f32_32x32x16_f16 a[64:79], v[8:11], v[100:103], a[64:79]
	v_mfma_f32_32x32x16_f16 a[48:63], v[12:15], v[100:103], a[48:63]
	s_waitcnt vmcnt(10)
	s_waitcnt lgkmcnt(0)
	s_barrier
	ds_read_b128 v[4:7], v98
	ds_read_b128 v[8:11], v98 offset:1024
	ds_read_b128 v[12:15], v98 offset:2048
	s_nop 0
	v_mfma_f32_32x32x16_f16 a[32:47], v[16:19], v[100:103], a[32:47]
	ds_read_b128 v[16:19], v98 offset:3072
	v_mfma_f32_32x32x16_f16 a[16:31], v[20:23], v[100:103], a[16:31]
	ds_read_b128 v[20:23], v98 offset:4096
	v_mfma_f32_32x32x16_f16 a[0:15], v[24:27], v[100:103], a[0:15]
	ds_read_b128 v[24:27], v98 offset:5120
	v_mfma_f32_32x32x16_f16 a[80:95], v[28:31], v[104:107], a[80:95]
	s_add_u32 m0, s46, 0xd3c0
	s_add_u32 s40, s40, 0x1800
	s_addc_u32 s41, s41, 0
	global_load_lds_dwordx4 v76, s[40:41]
	s_nop 0
	v_mfma_f32_32x32x16_f16 a[64:79], v[32:35], v[104:107], a[64:79]
	v_mfma_f32_32x32x16_f16 a[48:63], v[36:39], v[104:107], a[48:63]
	s_add_u32 m0, s47, 0xd3c0
	s_add_u32 s42, s42, 0x1800
	s_addc_u32 s43, s43, 0
	global_load_lds_dwordx4 v77, s[42:43]
	s_nop 0
	v_mfma_f32_32x32x16_f16 a[32:47], v[40:43], v[104:107], a[32:47]
	v_mfma_f32_32x32x16_f16 a[16:31], v[44:47], v[104:107], a[16:31]
	s_add_u32 m0, s48, 0xd3c0
	s_add_u32 s44, s44, 0x1800
	s_addc_u32 s45, s45, 0
	global_load_lds_dwordx4 v78, s[44:45]
	s_nop 0
	v_mfma_f32_32x32x16_f16 a[0:15], v[48:51], v[104:107], a[0:15]
	ds_read_b128 v[28:31], v98 offset:6144
	ds_read_b128 v[32:35], v98 offset:7168
	ds_read_b128 v[36:39], v98 offset:8192
	ds_read_b128 v[40:43], v98 offset:9216
	ds_read_b128 v[44:47], v98 offset:10240
	ds_read_b128 v[48:51], v98 offset:11264
	s_waitcnt lgkmcnt(6)
	s_nop 0
	v_mfma_f32_32x32x16_f16 a[80:95], v[4:7], v[108:111], a[80:95]
	s_waitcnt vmcnt(26)
	ds_write_b128 v81, v[116:119]
	ds_write_b128 v81, v[120:123] offset:1024
	ds_write_b128 v81, v[124:127] offset:2048
	ds_write_b128 v81, v[128:131] offset:3072
	s_nop 0
	v_mfma_f32_32x32x16_f16 a[64:79], v[8:11], v[108:111], a[64:79]
	ds_read_b128 v[52:55], v95
	ds_read_b128 v[56:59], v96
	ds_read_b128 v[60:63], v97
	ds_read_b128 v[0:3], v94
	v_mfma_f32_32x32x16_f16 a[48:63], v[12:15], v[108:111], a[48:63]
	global_load_dwordx4 v[116:119], v64, s[4:5] offset:1152
	global_load_dwordx4 v[120:123], v66, s[4:5] offset:1152
	global_load_dwordx4 v[124:127], v68, s[4:5] offset:1152
	global_load_dwordx4 v[128:131], v70, s[4:5] offset:1152
	s_waitcnt vmcnt(14)
	s_waitcnt lgkmcnt(8)
	s_barrier
	ds_read_b128 v[4:7], v84 offset:0
	ds_read_b128 v[8:11], v84 offset:1024
	ds_read_b128 v[12:15], v84 offset:2048
	s_nop 0
	v_mfma_f32_32x32x16_f16 a[32:47], v[16:19], v[108:111], a[32:47]
	ds_read_b128 v[16:19], v84 offset:3072
	v_mfma_f32_32x32x16_f16 a[16:31], v[20:23], v[108:111], a[16:31]
	ds_read_b128 v[20:23], v84 offset:4096
	v_mfma_f32_32x32x16_f16 a[0:15], v[24:27], v[108:111], a[0:15]
	ds_read_b128 v[24:27], v84 offset:5120
	v_mfma_f32_32x32x16_f16 a[80:95], v[28:31], v[112:115], a[80:95]
	s_add_u32 m0, s46, 0x103c0
	s_add_u32 s40, s40, 0x1800
	s_addc_u32 s41, s41, 0
	global_load_lds_dwordx4 v76, s[40:41]
	s_nop 0
	v_mfma_f32_32x32x16_f16 a[64:79], v[32:35], v[112:115], a[64:79]
	v_mfma_f32_32x32x16_f16 a[48:63], v[36:39], v[112:115], a[48:63]
	s_add_u32 m0, s47, 0x103c0
	s_add_u32 s42, s42, 0x1800
	s_addc_u32 s43, s43, 0
	global_load_lds_dwordx4 v77, s[42:43]
	s_nop 0
	v_mfma_f32_32x32x16_f16 a[32:47], v[40:43], v[112:115], a[32:47]
	v_mfma_f32_32x32x16_f16 a[16:31], v[44:47], v[112:115], a[16:31]
	s_add_u32 m0, s48, 0x103c0
	s_add_u32 s44, s44, 0x1800
	s_addc_u32 s45, s45, 0
	global_load_lds_dwordx4 v78, s[44:45]
	s_nop 0
	v_mfma_f32_32x32x16_f16 a[0:15], v[48:51], v[112:115], a[0:15]
	s_waitcnt lgkmcnt(6)
	ds_read_b128 v[28:31], v84 offset:6144
	ds_read_b128 v[32:35], v84 offset:7168
	ds_read_b128 v[36:39], v84 offset:8192
	ds_read_b128 v[40:43], v84 offset:9216
	ds_read_b128 v[44:47], v84 offset:10240
	ds_read_b128 v[48:51], v84 offset:11264
	s_waitcnt lgkmcnt(6)
	v_mfma_f32_32x32x16_f16 a[80:95], v[4:7], v[52:55], a[80:95]
	v_mfma_f32_32x32x16_f16 a[64:79], v[8:11], v[52:55], a[64:79]
	v_mfma_f32_32x32x16_f16 a[48:63], v[12:15], v[52:55], a[48:63]
	s_waitcnt vmcnt(10)
	s_waitcnt lgkmcnt(0)
	s_barrier
	ds_read_b128 v[4:7], v84 offset:12288
	ds_read_b128 v[8:11], v84 offset:13312
	ds_read_b128 v[12:15], v84 offset:14336
	s_nop 0
	v_mfma_f32_32x32x16_f16 a[32:47], v[16:19], v[52:55], a[32:47]
	ds_read_b128 v[16:19], v84 offset:15360
	v_mfma_f32_32x32x16_f16 a[16:31], v[20:23], v[52:55], a[16:31]
	ds_read_b128 v[20:23], v84 offset:16384
	v_mfma_f32_32x32x16_f16 a[0:15], v[24:27], v[52:55], a[0:15]
	ds_read_b128 v[24:27], v84 offset:17408
	v_mfma_f32_32x32x16_f16 a[80:95], v[28:31], v[56:59], a[80:95]
	s_add_u32 m0, s46, 0x0
	s_add_u32 s40, s40, 0x1800
	s_addc_u32 s41, s41, 0
	global_load_lds_dwordx4 v76, s[40:41]
	v_mfma_f32_32x32x16_f16 a[64:79], v[32:35], v[56:59], a[64:79]
	v_mfma_f32_32x32x16_f16 a[48:63], v[36:39], v[56:59], a[48:63]
	s_add_u32 m0, s47, 0x0
	s_add_u32 s42, s42, 0x1800
	s_addc_u32 s43, s43, 0
	global_load_lds_dwordx4 v77, s[42:43]
	v_mfma_f32_32x32x16_f16 a[32:47], v[40:43], v[56:59], a[32:47]
	v_mfma_f32_32x32x16_f16 a[16:31], v[44:47], v[56:59], a[16:31]
	s_add_u32 m0, s48, 0x0
	s_add_u32 s44, s44, 0x1800
	s_addc_u32 s45, s45, 0
	global_load_lds_dwordx4 v78, s[44:45]
	v_mfma_f32_32x32x16_f16 a[0:15], v[48:51], v[56:59], a[0:15]
	ds_read_b128 v[28:31], v84 offset:18432
	ds_read_b128 v[32:35], v84 offset:19456
	ds_read_b128 v[36:39], v84 offset:20480
	ds_read_b128 v[40:43], v84 offset:21504
	ds_read_b128 v[44:47], v84 offset:22528
	ds_read_b128 v[48:51], v84 offset:23552
	s_waitcnt lgkmcnt(6)
	s_nop 0
	v_mfma_f32_32x32x16_f16 a[80:95], v[4:7], v[60:63], a[80:95]
	s_waitcnt vmcnt(26)
	ds_write_b128 v81, v[132:135]
	ds_write_b128 v81, v[136:139] offset:1024
	ds_write_b128 v81, v[140:143] offset:2048
	ds_write_b128 v81, v[144:147] offset:3072
	s_nop 0
	v_mfma_f32_32x32x16_f16 a[64:79], v[8:11], v[60:63], a[64:79]
	ds_read_b128 v[100:103], v95
	ds_read_b128 v[104:107], v96
	ds_read_b128 v[108:111], v97
	ds_read_b128 v[112:115], v94
	v_mfma_f32_32x32x16_f16 a[48:63], v[12:15], v[60:63], a[48:63]
	global_load_dwordx4 v[132:135], v64, s[4:5] offset:1280
	global_load_dwordx4 v[136:139], v66, s[4:5] offset:1280
	global_load_dwordx4 v[140:143], v68, s[4:5] offset:1280
	global_load_dwordx4 v[144:147], v70, s[4:5] offset:1280
	s_waitcnt vmcnt(14)
	s_waitcnt lgkmcnt(8)
	s_barrier
	ds_read_b128 v[4:7], v84 offset:54208
	ds_read_b128 v[8:11], v84 offset:55232
	ds_read_b128 v[12:15], v84 offset:56256
	s_nop 0
	v_mfma_f32_32x32x16_f16 a[32:47], v[16:19], v[60:63], a[32:47]
	ds_read_b128 v[16:19], v84 offset:57280
	v_mfma_f32_32x32x16_f16 a[16:31], v[20:23], v[60:63], a[16:31]
	ds_read_b128 v[20:23], v84 offset:58304
	v_mfma_f32_32x32x16_f16 a[0:15], v[24:27], v[60:63], a[0:15]
	ds_read_b128 v[24:27], v84 offset:59328
	v_mfma_f32_32x32x16_f16 a[80:95], v[28:31], v[0:3], a[80:95]
	s_add_u32 m0, s46, 0x3000
	s_add_u32 s40, s40, 0x1800
	s_addc_u32 s41, s41, 0
	global_load_lds_dwordx4 v76, s[40:41]
	s_nop 0
	v_mfma_f32_32x32x16_f16 a[64:79], v[32:35], v[0:3], a[64:79]
	v_mfma_f32_32x32x16_f16 a[48:63], v[36:39], v[0:3], a[48:63]
	s_add_u32 m0, s47, 0x3000
	s_add_u32 s42, s42, 0x1800
	s_addc_u32 s43, s43, 0
	global_load_lds_dwordx4 v77, s[42:43]
	s_nop 0
	v_mfma_f32_32x32x16_f16 a[32:47], v[40:43], v[0:3], a[32:47]
	v_mfma_f32_32x32x16_f16 a[16:31], v[44:47], v[0:3], a[16:31]
	s_add_u32 m0, s48, 0x3000
	s_add_u32 s44, s44, 0x1800
	s_addc_u32 s45, s45, 0
	global_load_lds_dwordx4 v78, s[44:45]
	s_nop 0
	v_mfma_f32_32x32x16_f16 a[0:15], v[48:51], v[0:3], a[0:15]
	s_waitcnt lgkmcnt(6)
	ds_read_b128 v[28:31], v84 offset:60352
	ds_read_b128 v[32:35], v84 offset:61376
	ds_read_b128 v[36:39], v84 offset:62400
	ds_read_b128 v[40:43], v84 offset:63424
	ds_read_b128 v[44:47], v84 offset:64448
	ds_read_b128 v[48:51], v84 offset:65472
	s_waitcnt lgkmcnt(6)
	v_mfma_f32_32x32x16_f16 a[80:95], v[4:7], v[100:103], a[80:95]
	v_mfma_f32_32x32x16_f16 a[64:79], v[8:11], v[100:103], a[64:79]
	v_mfma_f32_32x32x16_f16 a[48:63], v[12:15], v[100:103], a[48:63]
	s_waitcnt vmcnt(10)
	s_waitcnt lgkmcnt(0)
	s_barrier
	ds_read_b128 v[4:7], v98
	ds_read_b128 v[8:11], v98 offset:1024
	ds_read_b128 v[12:15], v98 offset:2048
	s_nop 0
	v_mfma_f32_32x32x16_f16 a[32:47], v[16:19], v[100:103], a[32:47]
	ds_read_b128 v[16:19], v98 offset:3072
	v_mfma_f32_32x32x16_f16 a[16:31], v[20:23], v[100:103], a[16:31]
	ds_read_b128 v[20:23], v98 offset:4096
	v_mfma_f32_32x32x16_f16 a[0:15], v[24:27], v[100:103], a[0:15]
	ds_read_b128 v[24:27], v98 offset:5120
	v_mfma_f32_32x32x16_f16 a[80:95], v[28:31], v[104:107], a[80:95]
	s_add_u32 m0, s46, 0xd3c0
	s_add_u32 s40, s40, 0x1800
	s_addc_u32 s41, s41, 0
	global_load_lds_dwordx4 v76, s[40:41]
	s_nop 0
	v_mfma_f32_32x32x16_f16 a[64:79], v[32:35], v[104:107], a[64:79]
	v_mfma_f32_32x32x16_f16 a[48:63], v[36:39], v[104:107], a[48:63]
	s_add_u32 m0, s47, 0xd3c0
	s_add_u32 s42, s42, 0x1800
	s_addc_u32 s43, s43, 0
	global_load_lds_dwordx4 v77, s[42:43]
	s_nop 0
	v_mfma_f32_32x32x16_f16 a[32:47], v[40:43], v[104:107], a[32:47]
	v_mfma_f32_32x32x16_f16 a[16:31], v[44:47], v[104:107], a[16:31]
	s_add_u32 m0, s48, 0xd3c0
	s_add_u32 s44, s44, 0x1800
	s_addc_u32 s45, s45, 0
	global_load_lds_dwordx4 v78, s[44:45]
	s_nop 0
	v_mfma_f32_32x32x16_f16 a[0:15], v[48:51], v[104:107], a[0:15]
	ds_read_b128 v[28:31], v98 offset:6144
	ds_read_b128 v[32:35], v98 offset:7168
	ds_read_b128 v[36:39], v98 offset:8192
	ds_read_b128 v[40:43], v98 offset:9216
	ds_read_b128 v[44:47], v98 offset:10240
	ds_read_b128 v[48:51], v98 offset:11264
	s_waitcnt lgkmcnt(6)
	s_nop 0
	v_mfma_f32_32x32x16_f16 a[80:95], v[4:7], v[108:111], a[80:95]
	s_waitcnt vmcnt(26)
	ds_write_b128 v81, v[148:151]
	ds_write_b128 v81, v[152:155] offset:1024
	ds_write_b128 v81, v[156:159] offset:2048
	ds_write_b128 v81, v[72:75] offset:3072
	s_nop 0
	v_mfma_f32_32x32x16_f16 a[64:79], v[8:11], v[108:111], a[64:79]
	ds_read_b128 v[52:55], v95
	ds_read_b128 v[56:59], v96
	ds_read_b128 v[60:63], v97
	ds_read_b128 v[0:3], v94
	v_mfma_f32_32x32x16_f16 a[48:63], v[12:15], v[108:111], a[48:63]
	global_load_dwordx4 v[148:151], v64, s[4:5] offset:1408
	global_load_dwordx4 v[152:155], v66, s[4:5] offset:1408
	global_load_dwordx4 v[156:159], v68, s[4:5] offset:1408
	global_load_dwordx4 v[72:75], v70, s[4:5] offset:1408
	s_waitcnt vmcnt(14)
	s_waitcnt lgkmcnt(8)
	s_barrier
	ds_read_b128 v[4:7], v84 offset:0
	ds_read_b128 v[8:11], v84 offset:1024
	ds_read_b128 v[12:15], v84 offset:2048
	s_nop 0
	v_mfma_f32_32x32x16_f16 a[32:47], v[16:19], v[108:111], a[32:47]
	ds_read_b128 v[16:19], v84 offset:3072
	v_mfma_f32_32x32x16_f16 a[16:31], v[20:23], v[108:111], a[16:31]
	ds_read_b128 v[20:23], v84 offset:4096
	v_mfma_f32_32x32x16_f16 a[0:15], v[24:27], v[108:111], a[0:15]
	ds_read_b128 v[24:27], v84 offset:5120
	v_mfma_f32_32x32x16_f16 a[80:95], v[28:31], v[112:115], a[80:95]
	s_add_u32 m0, s46, 0x103c0
	s_add_u32 s40, s40, 0x1800
	s_addc_u32 s41, s41, 0
	global_load_lds_dwordx4 v76, s[40:41]
	s_nop 0
	v_mfma_f32_32x32x16_f16 a[64:79], v[32:35], v[112:115], a[64:79]
	v_mfma_f32_32x32x16_f16 a[48:63], v[36:39], v[112:115], a[48:63]
	s_add_u32 m0, s47, 0x103c0
	s_add_u32 s42, s42, 0x1800
	s_addc_u32 s43, s43, 0
	global_load_lds_dwordx4 v77, s[42:43]
	s_nop 0
	v_mfma_f32_32x32x16_f16 a[32:47], v[40:43], v[112:115], a[32:47]
	v_mfma_f32_32x32x16_f16 a[16:31], v[44:47], v[112:115], a[16:31]
	s_add_u32 m0, s48, 0x103c0
	s_add_u32 s44, s44, 0x1800
	s_addc_u32 s45, s45, 0
	global_load_lds_dwordx4 v78, s[44:45]
	s_nop 0
	v_mfma_f32_32x32x16_f16 a[0:15], v[48:51], v[112:115], a[0:15]
	s_waitcnt lgkmcnt(6)
	ds_read_b128 v[28:31], v84 offset:6144
	ds_read_b128 v[32:35], v84 offset:7168
	ds_read_b128 v[36:39], v84 offset:8192
	ds_read_b128 v[40:43], v84 offset:9216
	ds_read_b128 v[44:47], v84 offset:10240
	ds_read_b128 v[48:51], v84 offset:11264
	s_waitcnt lgkmcnt(6)
	v_mfma_f32_32x32x16_f16 a[80:95], v[4:7], v[52:55], a[80:95]
	v_mfma_f32_32x32x16_f16 a[64:79], v[8:11], v[52:55], a[64:79]
	v_mfma_f32_32x32x16_f16 a[48:63], v[12:15], v[52:55], a[48:63]
	s_waitcnt vmcnt(10)
	s_waitcnt lgkmcnt(0)
	s_barrier
	ds_read_b128 v[4:7], v84 offset:12288
	ds_read_b128 v[8:11], v84 offset:13312
	ds_read_b128 v[12:15], v84 offset:14336
	s_nop 0
	v_mfma_f32_32x32x16_f16 a[32:47], v[16:19], v[52:55], a[32:47]
	ds_read_b128 v[16:19], v84 offset:15360
	v_mfma_f32_32x32x16_f16 a[16:31], v[20:23], v[52:55], a[16:31]
	ds_read_b128 v[20:23], v84 offset:16384
	v_mfma_f32_32x32x16_f16 a[0:15], v[24:27], v[52:55], a[0:15]
	ds_read_b128 v[24:27], v84 offset:17408
	v_mfma_f32_32x32x16_f16 a[80:95], v[28:31], v[56:59], a[80:95]
	s_add_u32 m0, s46, 0x0
	s_add_u32 s40, s40, 0x1800
	s_addc_u32 s41, s41, 0
	global_load_lds_dwordx4 v76, s[40:41]
	v_mfma_f32_32x32x16_f16 a[64:79], v[32:35], v[56:59], a[64:79]
	v_mfma_f32_32x32x16_f16 a[48:63], v[36:39], v[56:59], a[48:63]
	s_add_u32 m0, s47, 0x0
	s_add_u32 s42, s42, 0x1800
	s_addc_u32 s43, s43, 0
	global_load_lds_dwordx4 v77, s[42:43]
	v_mfma_f32_32x32x16_f16 a[32:47], v[40:43], v[56:59], a[32:47]
	v_mfma_f32_32x32x16_f16 a[16:31], v[44:47], v[56:59], a[16:31]
	s_add_u32 m0, s48, 0x0
	s_add_u32 s44, s44, 0x1800
	s_addc_u32 s45, s45, 0
	global_load_lds_dwordx4 v78, s[44:45]
	v_mfma_f32_32x32x16_f16 a[0:15], v[48:51], v[56:59], a[0:15]
	ds_read_b128 v[28:31], v84 offset:18432
	ds_read_b128 v[32:35], v84 offset:19456
	ds_read_b128 v[36:39], v84 offset:20480
	ds_read_b128 v[40:43], v84 offset:21504
	ds_read_b128 v[44:47], v84 offset:22528
	ds_read_b128 v[48:51], v84 offset:23552
	s_waitcnt lgkmcnt(6)
	s_nop 0
	v_mfma_f32_32x32x16_f16 a[80:95], v[4:7], v[60:63], a[80:95]
	s_waitcnt vmcnt(26)
	ds_write_b128 v81, v[116:119]
	ds_write_b128 v81, v[120:123] offset:1024
	ds_write_b128 v81, v[124:127] offset:2048
	ds_write_b128 v81, v[128:131] offset:3072
	s_nop 0
	v_mfma_f32_32x32x16_f16 a[64:79], v[8:11], v[60:63], a[64:79]
	ds_read_b128 v[100:103], v95
	ds_read_b128 v[104:107], v96
	ds_read_b128 v[108:111], v97
	ds_read_b128 v[112:115], v94
	v_mfma_f32_32x32x16_f16 a[48:63], v[12:15], v[60:63], a[48:63]
	global_load_dwordx4 v[116:119], v64, s[4:5] offset:1440
	global_load_dwordx4 v[120:123], v66, s[4:5] offset:1440
	global_load_dwordx4 v[124:127], v68, s[4:5] offset:1440
	global_load_dwordx4 v[128:131], v70, s[4:5] offset:1440
	s_waitcnt vmcnt(14)
	s_waitcnt lgkmcnt(8)
	s_barrier
	ds_read_b128 v[4:7], v84 offset:54208
	ds_read_b128 v[8:11], v84 offset:55232
	ds_read_b128 v[12:15], v84 offset:56256
	s_nop 0
	v_mfma_f32_32x32x16_f16 a[32:47], v[16:19], v[60:63], a[32:47]
	ds_read_b128 v[16:19], v84 offset:57280
	v_mfma_f32_32x32x16_f16 a[16:31], v[20:23], v[60:63], a[16:31]
	ds_read_b128 v[20:23], v84 offset:58304
	v_mfma_f32_32x32x16_f16 a[0:15], v[24:27], v[60:63], a[0:15]
	ds_read_b128 v[24:27], v84 offset:59328
	v_mfma_f32_32x32x16_f16 a[80:95], v[28:31], v[0:3], a[80:95]
	s_add_u32 m0, s46, 0x3000
	s_add_u32 s40, s40, 0x1800
	s_addc_u32 s41, s41, 0
	global_load_lds_dwordx4 v76, s[40:41]
	s_nop 0
	v_mfma_f32_32x32x16_f16 a[64:79], v[32:35], v[0:3], a[64:79]
	v_mfma_f32_32x32x16_f16 a[48:63], v[36:39], v[0:3], a[48:63]
	s_add_u32 m0, s47, 0x3000
	s_add_u32 s42, s42, 0x1800
	s_addc_u32 s43, s43, 0
	global_load_lds_dwordx4 v77, s[42:43]
	s_nop 0
	v_mfma_f32_32x32x16_f16 a[32:47], v[40:43], v[0:3], a[32:47]
	v_mfma_f32_32x32x16_f16 a[16:31], v[44:47], v[0:3], a[16:31]
	s_add_u32 m0, s48, 0x3000
	s_add_u32 s44, s44, 0x1800
	s_addc_u32 s45, s45, 0
	global_load_lds_dwordx4 v78, s[44:45]
	s_nop 0
	v_mfma_f32_32x32x16_f16 a[0:15], v[48:51], v[0:3], a[0:15]
	s_waitcnt lgkmcnt(6)
	ds_read_b128 v[28:31], v84 offset:60352
	ds_read_b128 v[32:35], v84 offset:61376
	ds_read_b128 v[36:39], v84 offset:62400
	ds_read_b128 v[40:43], v84 offset:63424
	ds_read_b128 v[44:47], v84 offset:64448
	ds_read_b128 v[48:51], v84 offset:65472
	s_waitcnt lgkmcnt(6)
	v_mfma_f32_32x32x16_f16 a[80:95], v[4:7], v[100:103], a[80:95]
	v_mfma_f32_32x32x16_f16 a[64:79], v[8:11], v[100:103], a[64:79]
	v_mfma_f32_32x32x16_f16 a[48:63], v[12:15], v[100:103], a[48:63]
	s_waitcnt vmcnt(10)
	s_waitcnt lgkmcnt(0)
	s_barrier
	ds_read_b128 v[4:7], v98
	ds_read_b128 v[8:11], v98 offset:1024
	ds_read_b128 v[12:15], v98 offset:2048
	s_nop 0
	v_mfma_f32_32x32x16_f16 a[32:47], v[16:19], v[100:103], a[32:47]
	ds_read_b128 v[16:19], v98 offset:3072
	v_mfma_f32_32x32x16_f16 a[16:31], v[20:23], v[100:103], a[16:31]
	ds_read_b128 v[20:23], v98 offset:4096
	v_mfma_f32_32x32x16_f16 a[0:15], v[24:27], v[100:103], a[0:15]
	ds_read_b128 v[24:27], v98 offset:5120
	v_mfma_f32_32x32x16_f16 a[80:95], v[28:31], v[104:107], a[80:95]
	s_add_u32 m0, s46, 0xd3c0
	s_add_u32 s40, s40, 0x1800
	s_addc_u32 s41, s41, 0
	global_load_lds_dwordx4 v76, s[40:41]
	s_nop 0
	v_mfma_f32_32x32x16_f16 a[64:79], v[32:35], v[104:107], a[64:79]
	v_mfma_f32_32x32x16_f16 a[48:63], v[36:39], v[104:107], a[48:63]
	s_add_u32 m0, s47, 0xd3c0
	s_add_u32 s42, s42, 0x1800
	s_addc_u32 s43, s43, 0
	global_load_lds_dwordx4 v77, s[42:43]
	s_nop 0
	v_mfma_f32_32x32x16_f16 a[32:47], v[40:43], v[104:107], a[32:47]
	v_mfma_f32_32x32x16_f16 a[16:31], v[44:47], v[104:107], a[16:31]
	s_add_u32 m0, s48, 0xd3c0
	s_add_u32 s44, s44, 0x1800
	s_addc_u32 s45, s45, 0
	global_load_lds_dwordx4 v78, s[44:45]
	s_nop 0
	v_mfma_f32_32x32x16_f16 a[0:15], v[48:51], v[104:107], a[0:15]
	ds_read_b128 v[28:31], v98 offset:6144
	ds_read_b128 v[32:35], v98 offset:7168
	ds_read_b128 v[36:39], v98 offset:8192
	ds_read_b128 v[40:43], v98 offset:9216
	ds_read_b128 v[44:47], v98 offset:10240
	ds_read_b128 v[48:51], v98 offset:11264
	s_waitcnt lgkmcnt(6)
	s_nop 0
	v_mfma_f32_32x32x16_f16 a[80:95], v[4:7], v[108:111], a[80:95]
	s_waitcnt vmcnt(26)
	ds_write_b128 v81, v[132:135]
	ds_write_b128 v81, v[136:139] offset:1024
	ds_write_b128 v81, v[140:143] offset:2048
	ds_write_b128 v81, v[144:147] offset:3072
	s_nop 0
	v_mfma_f32_32x32x16_f16 a[64:79], v[8:11], v[108:111], a[64:79]
	ds_read_b128 v[52:55], v95
	ds_read_b128 v[56:59], v96
	ds_read_b128 v[60:63], v97
	ds_read_b128 v[0:3], v94
	v_mfma_f32_32x32x16_f16 a[48:63], v[12:15], v[108:111], a[48:63]
	s_waitcnt vmcnt(10)
	s_waitcnt lgkmcnt(8)
	s_barrier
	ds_read_b128 v[4:7], v84 offset:0
	ds_read_b128 v[8:11], v84 offset:1024
	ds_read_b128 v[12:15], v84 offset:2048
	s_nop 0
	v_mfma_f32_32x32x16_f16 a[32:47], v[16:19], v[108:111], a[32:47]
	ds_read_b128 v[16:19], v84 offset:3072
	v_mfma_f32_32x32x16_f16 a[16:31], v[20:23], v[108:111], a[16:31]
	ds_read_b128 v[20:23], v84 offset:4096
	v_mfma_f32_32x32x16_f16 a[0:15], v[24:27], v[108:111], a[0:15]
	ds_read_b128 v[24:27], v84 offset:5120
	v_mfma_f32_32x32x16_f16 a[80:95], v[28:31], v[112:115], a[80:95]
	s_add_u32 m0, s46, 0x103c0
	s_add_u32 s40, s40, 0x1800
	s_addc_u32 s41, s41, 0
	global_load_lds_dwordx4 v76, s[40:41]
	s_nop 0
	v_mfma_f32_32x32x16_f16 a[64:79], v[32:35], v[112:115], a[64:79]
	v_mfma_f32_32x32x16_f16 a[48:63], v[36:39], v[112:115], a[48:63]
	s_add_u32 m0, s47, 0x103c0
	s_add_u32 s42, s42, 0x1800
	s_addc_u32 s43, s43, 0
	global_load_lds_dwordx4 v77, s[42:43]
	s_nop 0
	v_mfma_f32_32x32x16_f16 a[32:47], v[40:43], v[112:115], a[32:47]
	v_mfma_f32_32x32x16_f16 a[16:31], v[44:47], v[112:115], a[16:31]
	s_add_u32 m0, s48, 0x103c0
	s_add_u32 s44, s44, 0x1800
	s_addc_u32 s45, s45, 0
	global_load_lds_dwordx4 v78, s[44:45]
	s_nop 0
	v_mfma_f32_32x32x16_f16 a[0:15], v[48:51], v[112:115], a[0:15]
	s_waitcnt lgkmcnt(6)
	ds_read_b128 v[28:31], v84 offset:6144
	ds_read_b128 v[32:35], v84 offset:7168
	ds_read_b128 v[36:39], v84 offset:8192
	ds_read_b128 v[40:43], v84 offset:9216
	ds_read_b128 v[44:47], v84 offset:10240
	ds_read_b128 v[48:51], v84 offset:11264
	s_waitcnt lgkmcnt(6)
	v_mfma_f32_32x32x16_f16 a[80:95], v[4:7], v[52:55], a[80:95]
	v_mfma_f32_32x32x16_f16 a[64:79], v[8:11], v[52:55], a[64:79]
	v_mfma_f32_32x32x16_f16 a[48:63], v[12:15], v[52:55], a[48:63]
	s_waitcnt vmcnt(6)
	s_waitcnt lgkmcnt(0)
	s_barrier
	ds_read_b128 v[4:7], v84 offset:12288
	ds_read_b128 v[8:11], v84 offset:13312
	ds_read_b128 v[12:15], v84 offset:14336
	s_nop 0
	v_mfma_f32_32x32x16_f16 a[32:47], v[16:19], v[52:55], a[32:47]
	ds_read_b128 v[16:19], v84 offset:15360
	v_mfma_f32_32x32x16_f16 a[16:31], v[20:23], v[52:55], a[16:31]
	ds_read_b128 v[20:23], v84 offset:16384
	v_mfma_f32_32x32x16_f16 a[0:15], v[24:27], v[52:55], a[0:15]
	ds_read_b128 v[24:27], v84 offset:17408
	v_mfma_f32_32x32x16_f16 a[80:95], v[28:31], v[56:59], a[80:95]
	s_add_u32 m0, s46, 0x0
	s_add_u32 s40, s40, 0x1800
	s_addc_u32 s41, s41, 0
	global_load_lds_dwordx4 v76, s[40:41]
	v_mfma_f32_32x32x16_f16 a[64:79], v[32:35], v[56:59], a[64:79]
	v_mfma_f32_32x32x16_f16 a[48:63], v[36:39], v[56:59], a[48:63]
	s_add_u32 m0, s47, 0x0
	s_add_u32 s42, s42, s49
	s_addc_u32 s43, s43, 0
	global_load_lds_dwordx4 v77, s[42:43]
	s_nop 0
	v_mfma_f32_32x32x16_f16 a[32:47], v[40:43], v[56:59], a[32:47]
	v_mfma_f32_32x32x16_f16 a[16:31], v[44:47], v[56:59], a[16:31]
	s_add_u32 m0, s48, 0x0
	s_add_u32 s44, s44, 0xc00
	s_addc_u32 s45, s45, 0
	global_load_lds_dwordx4 v78, s[44:45]
	v_mfma_f32_32x32x16_f16 a[0:15], v[48:51], v[56:59], a[0:15]
	ds_read_b128 v[28:31], v84 offset:18432
	ds_read_b128 v[32:35], v84 offset:19456
	ds_read_b128 v[36:39], v84 offset:20480
	ds_read_b128 v[40:43], v84 offset:21504
	ds_read_b128 v[44:47], v84 offset:22528
	ds_read_b128 v[48:51], v84 offset:23552
	s_waitcnt lgkmcnt(6)
	s_nop 0
	v_mfma_f32_32x32x16_f16 a[80:95], v[4:7], v[60:63], a[80:95]
	s_waitcnt vmcnt(22)
	ds_write_b128 v81, v[148:151]
	ds_write_b128 v81, v[152:155] offset:1024
	ds_write_b128 v81, v[156:159] offset:2048
	ds_write_b128 v81, v[72:75] offset:3072
	s_nop 0
	v_mfma_f32_32x32x16_f16 a[64:79], v[8:11], v[60:63], a[64:79]
	ds_read_b128 v[100:103], v95
	ds_read_b128 v[104:107], v96
	ds_read_b128 v[108:111], v97
	ds_read_b128 v[112:115], v94
	v_mfma_f32_32x32x16_f16 a[48:63], v[12:15], v[60:63], a[48:63]
	s_waitcnt vmcnt(6)
	s_waitcnt lgkmcnt(8)
	s_barrier
	ds_read_b128 v[4:7], v84 offset:54208
	ds_read_b128 v[8:11], v84 offset:55232
	ds_read_b128 v[12:15], v84 offset:56256
	s_nop 0
	v_mfma_f32_32x32x16_f16 a[32:47], v[16:19], v[60:63], a[32:47]
	ds_read_b128 v[16:19], v84 offset:57280
	v_mfma_f32_32x32x16_f16 a[16:31], v[20:23], v[60:63], a[16:31]
	ds_read_b128 v[20:23], v84 offset:58304
	v_mfma_f32_32x32x16_f16 a[0:15], v[24:27], v[60:63], a[0:15]
	ds_read_b128 v[24:27], v84 offset:59328
	v_mfma_f32_32x32x16_f16 a[80:95], v[28:31], v[0:3], a[80:95]
	v_mfma_f32_32x32x16_f16 a[64:79], v[32:35], v[0:3], a[64:79]
	v_mfma_f32_32x32x16_f16 a[48:63], v[36:39], v[0:3], a[48:63]
	v_mfma_f32_32x32x16_f16 a[32:47], v[40:43], v[0:3], a[32:47]
	v_mfma_f32_32x32x16_f16 a[16:31], v[44:47], v[0:3], a[16:31]
	v_mfma_f32_32x32x16_f16 a[0:15], v[48:51], v[0:3], a[0:15]
	s_waitcnt lgkmcnt(6)
	ds_read_b128 v[28:31], v84 offset:60352
	ds_read_b128 v[32:35], v84 offset:61376
	ds_read_b128 v[36:39], v84 offset:62400
	ds_read_b128 v[40:43], v84 offset:63424
	ds_read_b128 v[44:47], v84 offset:64448
	ds_read_b128 v[48:51], v84 offset:65472
	s_waitcnt lgkmcnt(6)
	v_mfma_f32_32x32x16_f16 a[80:95], v[4:7], v[100:103], a[80:95]
	v_mfma_f32_32x32x16_f16 a[64:79], v[8:11], v[100:103], a[64:79]
	v_mfma_f32_32x32x16_f16 a[48:63], v[12:15], v[100:103], a[48:63]
	s_waitcnt vmcnt(3)
	s_waitcnt lgkmcnt(0)
	s_barrier
	ds_read_b128 v[4:7], v98
	ds_read_b128 v[8:11], v98 offset:1024
	ds_read_b128 v[12:15], v98 offset:2048
	s_nop 0
	v_mfma_f32_32x32x16_f16 a[32:47], v[16:19], v[100:103], a[32:47]
	ds_read_b128 v[16:19], v98 offset:3072
	v_mfma_f32_32x32x16_f16 a[16:31], v[20:23], v[100:103], a[16:31]
	ds_read_b128 v[20:23], v98 offset:4096
	v_mfma_f32_32x32x16_f16 a[0:15], v[24:27], v[100:103], a[0:15]
	ds_read_b128 v[24:27], v98 offset:5120
	v_mfma_f32_32x32x16_f16 a[80:95], v[28:31], v[104:107], a[80:95]
	v_mfma_f32_32x32x16_f16 a[64:79], v[32:35], v[104:107], a[64:79]
	v_mfma_f32_32x32x16_f16 a[48:63], v[36:39], v[104:107], a[48:63]
	v_mfma_f32_32x32x16_f16 a[32:47], v[40:43], v[104:107], a[32:47]
	v_mfma_f32_32x32x16_f16 a[16:31], v[44:47], v[104:107], a[16:31]
	v_mfma_f32_32x32x16_f16 a[0:15], v[48:51], v[104:107], a[0:15]
	ds_read_b128 v[28:31], v98 offset:6144
	ds_read_b128 v[32:35], v98 offset:7168
	ds_read_b128 v[36:39], v98 offset:8192
	ds_read_b128 v[40:43], v98 offset:9216
	ds_read_b128 v[44:47], v98 offset:10240
	ds_read_b128 v[48:51], v98 offset:11264
	s_waitcnt lgkmcnt(6)
	s_nop 0
	v_mfma_f32_32x32x16_f16 a[80:95], v[4:7], v[108:111], a[80:95]
	s_waitcnt vmcnt(12)
	ds_write_b128 v81, v[116:119]
	ds_write_b128 v81, v[120:123] offset:1024
	ds_write_b128 v81, v[124:127] offset:2048
	ds_write_b128 v81, v[128:131] offset:3072
	s_nop 0
	v_mfma_f32_32x32x16_f16 a[64:79], v[8:11], v[108:111], a[64:79]
	ds_read_b128 v[0:3], v94
	v_mfma_f32_32x32x16_f16 a[48:63], v[12:15], v[108:111], a[48:63]
	s_waitcnt vmcnt(0)
	s_waitcnt lgkmcnt(5)
	s_barrier
	ds_read_b128 v[4:7], v84 offset:0
	ds_read_b128 v[8:11], v84 offset:1024
	ds_read_b128 v[12:15], v84 offset:2048
	s_nop 0
	v_mfma_f32_32x32x16_f16 a[32:47], v[16:19], v[108:111], a[32:47]
	ds_read_b128 v[16:19], v84 offset:3072
	v_mfma_f32_32x32x16_f16 a[16:31], v[20:23], v[108:111], a[16:31]
	ds_read_b128 v[20:23], v84 offset:4096
	v_mfma_f32_32x32x16_f16 a[0:15], v[24:27], v[108:111], a[0:15]
	ds_read_b128 v[24:27], v84 offset:5120
	v_mfma_f32_32x32x16_f16 a[80:95], v[28:31], v[112:115], a[80:95]
	v_mfma_f32_32x32x16_f16 a[64:79], v[32:35], v[112:115], a[64:79]
	v_mfma_f32_32x32x16_f16 a[48:63], v[36:39], v[112:115], a[48:63]
	v_mfma_f32_32x32x16_f16 a[32:47], v[40:43], v[112:115], a[32:47]
	v_mfma_f32_32x32x16_f16 a[16:31], v[44:47], v[112:115], a[16:31]
	v_mfma_f32_32x32x16_f16 a[0:15], v[48:51], v[112:115], a[0:15]
	s_waitcnt lgkmcnt(0)
	v_mfma_f32_32x32x16_f16 a[80:95], v[4:7], v[0:3], a[80:95]
	v_mfma_f32_32x32x16_f16 a[16:31], v[20:23], v[0:3], a[16:31]
	v_lshlrev_b32_e32 v22, 4, v85
	v_mfma_f32_32x32x16_f16 a[64:79], v[8:11], v[0:3], a[64:79]
	v_mfma_f32_32x32x16_f16 a[48:63], v[12:15], v[0:3], a[48:63]
	s_nop 7
	v_accvgpr_read_b32 v13, a88
	v_mfma_f32_32x32x16_f16 a[32:47], v[16:19], v[0:3], a[32:47]
	v_accvgpr_read_b32 v17, a92
	v_mfma_f32_32x32x16_f16 a[0:15], v[24:27], v[0:3], a[0:15]
	ds_read_b128 v[2:5], v22 offset:53248
	ds_read_b128 v[6:9], v22 offset:53280
	v_accvgpr_read_b32 v1, a80
	v_lshlrev_b32_e32 v0, 4, v92
	s_waitcnt lgkmcnt(1)
	v_add_f32_e32 v1, v1, v2
	v_accvgpr_read_b32 v2, a81
	v_add_f32_e32 v2, v3, v2
	v_max_f32_e32 v10, 0, v2
	v_accvgpr_read_b32 v2, a82
	v_add_f32_e32 v2, v4, v2
	v_max_f32_e32 v11, 0, v2
	v_accvgpr_read_b32 v2, a83
	v_add_f32_e32 v2, v5, v2
	v_max_f32_e32 v12, 0, v2
	v_accvgpr_read_b32 v2, a84
	s_waitcnt lgkmcnt(0)
	v_add_f32_e32 v2, v2, v6
	v_max_f32_e32 v6, 0, v2
	v_accvgpr_read_b32 v2, a85
	v_add_f32_e32 v2, v7, v2
	v_max_f32_e32 v7, 0, v2
	v_accvgpr_read_b32 v2, a86
	v_add_f32_e32 v2, v8, v2
	v_max_f32_e32 v8, 0, v2
	v_accvgpr_read_b32 v2, a87
	v_add_f32_e32 v2, v9, v2
	v_max_f32_e32 v9, 0, v2
	ds_read_b128 v[2:5], v22 offset:53312
	v_max_f32_e32 v1, 0, v1
	s_waitcnt lgkmcnt(0)
	v_add_f32_e32 v2, v13, v2
	v_max_f32_e32 v13, 0, v2
	v_accvgpr_read_b32 v2, a89
	v_add_f32_e32 v2, v3, v2
	v_max_f32_e32 v14, 0, v2
	v_accvgpr_read_b32 v2, a90
	v_add_f32_e32 v2, v4, v2
	v_max_f32_e32 v15, 0, v2
	v_accvgpr_read_b32 v2, a91
	v_add_f32_e32 v2, v5, v2
	v_max_f32_e32 v16, 0, v2
	ds_read_b128 v[2:5], v22 offset:53344
	s_waitcnt lgkmcnt(0)
	v_add_f32_e32 v2, v17, v2
	v_max_f32_e32 v17, 0, v2
	v_accvgpr_read_b32 v2, a93
	v_add_f32_e32 v2, v3, v2
	v_max_f32_e32 v18, 0, v2
	v_accvgpr_read_b32 v2, a94
	v_add_f32_e32 v2, v4, v2
	v_max_f32_e32 v19, 0, v2
	v_accvgpr_read_b32 v2, a95
	v_add_f32_e32 v2, v5, v2
	v_cvt_pk_f16_f32 v5, v8, v9
	v_cvt_pk_f16_f32 v4, v6, v7
	ds_read_b128 v[6:9], v0 offset:40960
	v_max_f32_e32 v20, 0, v2
	v_cvt_pk_f16_f32 v3, v11, v12
	v_cvt_pk_f16_f32 v2, v1, v10
	v_accvgpr_read_b32 v1, a64
	s_waitcnt lgkmcnt(0)
	v_mfma_f32_32x32x16_f16 a[80:95], v[6:9], v[2:5], 0
	ds_read_b128 v[6:9], v0 offset:41984
	v_cvt_pk_f16_f32 v5, v19, v20
	v_cvt_pk_f16_f32 v4, v17, v18
	v_cvt_pk_f16_f32 v3, v15, v16
	v_cvt_pk_f16_f32 v2, v13, v14
	v_accvgpr_read_b32 v13, a72
	v_accvgpr_read_b32 v17, a76
	s_waitcnt lgkmcnt(0)
	v_mfma_f32_32x32x16_f16 a[80:95], v[6:9], v[2:5], a[80:95]
	ds_read_b128 v[2:5], v22 offset:53376
	v_accvgpr_read_b32 v9, a68
	s_waitcnt lgkmcnt(0)
	v_add_f32_e32 v1, v1, v2
	v_accvgpr_read_b32 v2, a65
	v_add_f32_e32 v2, v3, v2
	v_max_f32_e32 v6, 0, v2
	v_accvgpr_read_b32 v2, a66
	v_add_f32_e32 v2, v4, v2
	v_max_f32_e32 v7, 0, v2
	v_accvgpr_read_b32 v2, a67
	v_add_f32_e32 v2, v5, v2
	v_max_f32_e32 v8, 0, v2
	ds_read_b128 v[2:5], v22 offset:53408
	v_max_f32_e32 v1, 0, v1
	s_waitcnt lgkmcnt(0)
	v_add_f32_e32 v2, v9, v2
	v_max_f32_e32 v9, 0, v2
	v_accvgpr_read_b32 v2, a69
	v_add_f32_e32 v2, v3, v2
	v_max_f32_e32 v10, 0, v2
	v_accvgpr_read_b32 v2, a70
	v_add_f32_e32 v2, v4, v2
	v_max_f32_e32 v11, 0, v2
	v_accvgpr_read_b32 v2, a71
	v_add_f32_e32 v2, v5, v2
	v_max_f32_e32 v12, 0, v2
	ds_read_b128 v[2:5], v22 offset:53440
	s_waitcnt lgkmcnt(0)
	v_add_f32_e32 v2, v13, v2
	v_max_f32_e32 v13, 0, v2
	v_accvgpr_read_b32 v2, a73
	v_add_f32_e32 v2, v3, v2
	v_max_f32_e32 v14, 0, v2
	v_accvgpr_read_b32 v2, a74
	v_add_f32_e32 v2, v4, v2
	v_max_f32_e32 v15, 0, v2
	v_accvgpr_read_b32 v2, a75
	v_add_f32_e32 v2, v5, v2
	v_max_f32_e32 v16, 0, v2
	ds_read_b128 v[2:5], v22 offset:53472
	s_waitcnt lgkmcnt(0)
	v_add_f32_e32 v2, v17, v2
	v_max_f32_e32 v17, 0, v2
	v_accvgpr_read_b32 v2, a77
	v_add_f32_e32 v2, v3, v2
	v_max_f32_e32 v18, 0, v2
	v_accvgpr_read_b32 v2, a78
	v_add_f32_e32 v2, v4, v2
	v_max_f32_e32 v19, 0, v2
	v_accvgpr_read_b32 v2, a79
	v_add_f32_e32 v2, v5, v2
	v_max_f32_e32 v20, 0, v2
	v_cvt_pk_f16_f32 v4, v9, v10
	v_cvt_pk_f16_f32 v3, v7, v8
	v_cvt_pk_f16_f32 v2, v1, v6
	ds_read_b128 v[6:9], v0 offset:43008
	v_cvt_pk_f16_f32 v5, v11, v12
	v_accvgpr_read_b32 v1, a48
	s_waitcnt lgkmcnt(0)
	v_mfma_f32_32x32x16_f16 a[80:95], v[6:9], v[2:5], a[80:95]
	ds_read_b128 v[6:9], v0 offset:44032
	v_cvt_pk_f16_f32 v5, v19, v20
	v_cvt_pk_f16_f32 v4, v17, v18
	v_cvt_pk_f16_f32 v3, v15, v16
	v_cvt_pk_f16_f32 v2, v13, v14
	v_accvgpr_read_b32 v13, a56
	v_accvgpr_read_b32 v17, a60
	s_waitcnt lgkmcnt(0)
	v_mfma_f32_32x32x16_f16 a[80:95], v[6:9], v[2:5], a[80:95]
	ds_read_b128 v[2:5], v22 offset:53504
	v_accvgpr_read_b32 v9, a52
	s_waitcnt lgkmcnt(0)
	v_add_f32_e32 v1, v1, v2
	v_accvgpr_read_b32 v2, a49
	v_add_f32_e32 v2, v3, v2
	v_max_f32_e32 v6, 0, v2
	v_accvgpr_read_b32 v2, a50
	v_add_f32_e32 v2, v4, v2
	v_max_f32_e32 v7, 0, v2
	v_accvgpr_read_b32 v2, a51
	v_add_f32_e32 v2, v5, v2
	v_max_f32_e32 v8, 0, v2
	ds_read_b128 v[2:5], v22 offset:53536
	v_max_f32_e32 v1, 0, v1
	s_waitcnt lgkmcnt(0)
	v_add_f32_e32 v2, v9, v2
	v_max_f32_e32 v9, 0, v2
	v_accvgpr_read_b32 v2, a53
	v_add_f32_e32 v2, v3, v2
	v_max_f32_e32 v10, 0, v2
	v_accvgpr_read_b32 v2, a54
	v_add_f32_e32 v2, v4, v2
	v_max_f32_e32 v11, 0, v2
	v_accvgpr_read_b32 v2, a55
	v_add_f32_e32 v2, v5, v2
	v_max_f32_e32 v12, 0, v2
	ds_read_b128 v[2:5], v22 offset:53568
	s_waitcnt lgkmcnt(0)
	v_add_f32_e32 v2, v13, v2
	v_max_f32_e32 v13, 0, v2
	v_accvgpr_read_b32 v2, a57
	v_add_f32_e32 v2, v3, v2
	v_max_f32_e32 v14, 0, v2
	v_accvgpr_read_b32 v2, a58
	v_add_f32_e32 v2, v4, v2
	v_max_f32_e32 v15, 0, v2
	v_accvgpr_read_b32 v2, a59
	v_add_f32_e32 v2, v5, v2
	v_max_f32_e32 v16, 0, v2
	ds_read_b128 v[2:5], v22 offset:53600
	s_waitcnt lgkmcnt(0)
	v_add_f32_e32 v2, v17, v2
	v_max_f32_e32 v17, 0, v2
	v_accvgpr_read_b32 v2, a61
	v_add_f32_e32 v2, v3, v2
	v_max_f32_e32 v18, 0, v2
	v_accvgpr_read_b32 v2, a62
	v_add_f32_e32 v2, v4, v2
	v_max_f32_e32 v19, 0, v2
	v_accvgpr_read_b32 v2, a63
	v_add_f32_e32 v2, v5, v2
	v_max_f32_e32 v20, 0, v2
	v_cvt_pk_f16_f32 v4, v9, v10
	v_cvt_pk_f16_f32 v3, v7, v8
	v_cvt_pk_f16_f32 v2, v1, v6
	ds_read_b128 v[6:9], v0 offset:45056
	v_cvt_pk_f16_f32 v5, v11, v12
	v_accvgpr_read_b32 v1, a32
	s_waitcnt lgkmcnt(0)
	v_mfma_f32_32x32x16_f16 a[80:95], v[6:9], v[2:5], a[80:95]
	ds_read_b128 v[6:9], v0 offset:46080
	v_cvt_pk_f16_f32 v5, v19, v20
	v_cvt_pk_f16_f32 v4, v17, v18
	v_cvt_pk_f16_f32 v3, v15, v16
	v_cvt_pk_f16_f32 v2, v13, v14
	v_accvgpr_read_b32 v13, a40
	v_accvgpr_read_b32 v17, a44
	s_waitcnt lgkmcnt(0)
	v_mfma_f32_32x32x16_f16 a[80:95], v[6:9], v[2:5], a[80:95]
	ds_read_b128 v[2:5], v22 offset:53632
	v_accvgpr_read_b32 v9, a36
	s_waitcnt lgkmcnt(0)
	v_add_f32_e32 v1, v1, v2
	v_accvgpr_read_b32 v2, a33
	v_add_f32_e32 v2, v3, v2
	v_max_f32_e32 v6, 0, v2
	v_accvgpr_read_b32 v2, a34
	v_add_f32_e32 v2, v4, v2
	v_max_f32_e32 v7, 0, v2
	v_accvgpr_read_b32 v2, a35
	v_add_f32_e32 v2, v5, v2
	v_max_f32_e32 v8, 0, v2
	ds_read_b128 v[2:5], v22 offset:53664
	v_max_f32_e32 v1, 0, v1
	s_waitcnt lgkmcnt(0)
	v_add_f32_e32 v2, v9, v2
	v_max_f32_e32 v9, 0, v2
	v_accvgpr_read_b32 v2, a37
	v_add_f32_e32 v2, v3, v2
	v_max_f32_e32 v10, 0, v2
	v_accvgpr_read_b32 v2, a38
	v_add_f32_e32 v2, v4, v2
	v_max_f32_e32 v11, 0, v2
	v_accvgpr_read_b32 v2, a39
	v_add_f32_e32 v2, v5, v2
	v_max_f32_e32 v12, 0, v2
	ds_read_b128 v[2:5], v22 offset:53696
	s_waitcnt lgkmcnt(0)
	v_add_f32_e32 v2, v13, v2
	v_max_f32_e32 v13, 0, v2
	v_accvgpr_read_b32 v2, a41
	v_add_f32_e32 v2, v3, v2
	v_max_f32_e32 v14, 0, v2
	v_accvgpr_read_b32 v2, a42
	v_add_f32_e32 v2, v4, v2
	v_max_f32_e32 v15, 0, v2
	v_accvgpr_read_b32 v2, a43
	v_add_f32_e32 v2, v5, v2
	v_max_f32_e32 v16, 0, v2
	ds_read_b128 v[2:5], v22 offset:53728
	s_waitcnt lgkmcnt(0)
	v_add_f32_e32 v2, v17, v2
	v_max_f32_e32 v17, 0, v2
	v_accvgpr_read_b32 v2, a45
	v_add_f32_e32 v2, v3, v2
	v_max_f32_e32 v18, 0, v2
	v_accvgpr_read_b32 v2, a46
	v_add_f32_e32 v2, v4, v2
	v_max_f32_e32 v19, 0, v2
	v_accvgpr_read_b32 v2, a47
	v_add_f32_e32 v2, v5, v2
	v_max_f32_e32 v20, 0, v2
	v_cvt_pk_f16_f32 v4, v9, v10
	v_cvt_pk_f16_f32 v3, v7, v8
	v_cvt_pk_f16_f32 v2, v1, v6
	ds_read_b128 v[6:9], v0 offset:47104
	v_cvt_pk_f16_f32 v5, v11, v12
	v_accvgpr_read_b32 v1, a16
	s_waitcnt lgkmcnt(0)
	v_mfma_f32_32x32x16_f16 a[32:47], v[6:9], v[2:5], 0
	ds_read_b128 v[6:9], v0 offset:48128
	v_cvt_pk_f16_f32 v5, v19, v20
	v_cvt_pk_f16_f32 v4, v17, v18
	v_cvt_pk_f16_f32 v3, v15, v16
	v_cvt_pk_f16_f32 v2, v13, v14
	v_accvgpr_read_b32 v13, a24
	v_accvgpr_read_b32 v17, a28
	s_waitcnt lgkmcnt(0)
	v_mfma_f32_32x32x16_f16 a[32:47], v[6:9], v[2:5], a[32:47]
	ds_read_b128 v[2:5], v22 offset:53760
	v_accvgpr_read_b32 v9, a20
	s_waitcnt lgkmcnt(0)
	v_add_f32_e32 v1, v1, v2
	v_accvgpr_read_b32 v2, a17
	v_add_f32_e32 v2, v3, v2
	v_max_f32_e32 v6, 0, v2
	v_accvgpr_read_b32 v2, a18
	v_add_f32_e32 v2, v4, v2
	v_max_f32_e32 v7, 0, v2
	v_accvgpr_read_b32 v2, a19
	v_add_f32_e32 v2, v5, v2
	v_max_f32_e32 v8, 0, v2
	ds_read_b128 v[2:5], v22 offset:53792
	v_max_f32_e32 v1, 0, v1
	s_waitcnt lgkmcnt(0)
	v_add_f32_e32 v2, v9, v2
	v_max_f32_e32 v9, 0, v2
	v_accvgpr_read_b32 v2, a21
	v_add_f32_e32 v2, v3, v2
	v_max_f32_e32 v10, 0, v2
	v_accvgpr_read_b32 v2, a22
	v_add_f32_e32 v2, v4, v2
	v_max_f32_e32 v11, 0, v2
	v_accvgpr_read_b32 v2, a23
	v_add_f32_e32 v2, v5, v2
	v_max_f32_e32 v12, 0, v2
	ds_read_b128 v[2:5], v22 offset:53824
	s_waitcnt lgkmcnt(0)
	v_add_f32_e32 v2, v13, v2
	v_max_f32_e32 v13, 0, v2
	v_accvgpr_read_b32 v2, a25
	v_add_f32_e32 v2, v3, v2
	v_max_f32_e32 v14, 0, v2
	v_accvgpr_read_b32 v2, a26
	v_add_f32_e32 v2, v4, v2
	v_max_f32_e32 v15, 0, v2
	v_accvgpr_read_b32 v2, a27
	v_add_f32_e32 v2, v5, v2
	v_max_f32_e32 v16, 0, v2
	ds_read_b128 v[2:5], v22 offset:53856
	s_waitcnt lgkmcnt(0)
	v_add_f32_e32 v2, v17, v2
	v_max_f32_e32 v17, 0, v2
	v_accvgpr_read_b32 v2, a29
	v_add_f32_e32 v2, v3, v2
	v_max_f32_e32 v18, 0, v2
	v_accvgpr_read_b32 v2, a30
	v_add_f32_e32 v2, v4, v2
	v_max_f32_e32 v19, 0, v2
	v_accvgpr_read_b32 v2, a31
	v_add_f32_e32 v2, v5, v2
	v_max_f32_e32 v20, 0, v2
	v_cvt_pk_f16_f32 v4, v9, v10
	v_cvt_pk_f16_f32 v3, v7, v8
	v_cvt_pk_f16_f32 v2, v1, v6
	ds_read_b128 v[6:9], v0 offset:49152
	v_cvt_pk_f16_f32 v5, v11, v12
	v_accvgpr_read_b32 v1, a0
	s_waitcnt lgkmcnt(0)
	v_mfma_f32_32x32x16_f16 a[32:47], v[6:9], v[2:5], a[32:47]
	ds_read_b128 v[6:9], v0 offset:50176
	v_cvt_pk_f16_f32 v5, v19, v20
	v_cvt_pk_f16_f32 v4, v17, v18
	v_cvt_pk_f16_f32 v3, v15, v16
	v_cvt_pk_f16_f32 v2, v13, v14
	v_accvgpr_read_b32 v13, a8
	v_accvgpr_read_b32 v17, a12
	s_waitcnt lgkmcnt(0)
	v_mfma_f32_32x32x16_f16 a[32:47], v[6:9], v[2:5], a[32:47]
	ds_read_b128 v[2:5], v22 offset:53888
	v_accvgpr_read_b32 v9, a4
	s_waitcnt lgkmcnt(0)
	v_add_f32_e32 v1, v1, v2
	v_accvgpr_read_b32 v2, a1
	v_add_f32_e32 v2, v3, v2
	v_max_f32_e32 v6, 0, v2
	v_accvgpr_read_b32 v2, a2
	v_add_f32_e32 v2, v4, v2
	v_max_f32_e32 v7, 0, v2
	v_accvgpr_read_b32 v2, a3
	v_add_f32_e32 v2, v5, v2
	v_max_f32_e32 v8, 0, v2
	ds_read_b128 v[2:5], v22 offset:53920
	v_max_f32_e32 v1, 0, v1
	s_waitcnt lgkmcnt(0)
	v_add_f32_e32 v2, v9, v2
	v_max_f32_e32 v9, 0, v2
	v_accvgpr_read_b32 v2, a5
	v_add_f32_e32 v2, v3, v2
	v_max_f32_e32 v10, 0, v2
	v_accvgpr_read_b32 v2, a6
	v_add_f32_e32 v2, v4, v2
	v_max_f32_e32 v11, 0, v2
	v_accvgpr_read_b32 v2, a7
	v_add_f32_e32 v2, v5, v2
	v_max_f32_e32 v12, 0, v2
	ds_read_b128 v[2:5], v22 offset:53952
	s_waitcnt lgkmcnt(0)
	v_add_f32_e32 v2, v13, v2
	v_max_f32_e32 v13, 0, v2
	v_accvgpr_read_b32 v2, a9
	v_add_f32_e32 v2, v3, v2
	v_max_f32_e32 v14, 0, v2
	v_accvgpr_read_b32 v2, a10
	v_add_f32_e32 v2, v4, v2
	v_max_f32_e32 v15, 0, v2
	v_accvgpr_read_b32 v2, a11
	v_add_f32_e32 v2, v5, v2
	v_max_f32_e32 v16, 0, v2
	ds_read_b128 v[2:5], v22 offset:53984
	s_waitcnt lgkmcnt(0)
	v_add_f32_e32 v2, v17, v2
	v_max_f32_e32 v17, 0, v2
	v_accvgpr_read_b32 v2, a13
	v_add_f32_e32 v2, v3, v2
	v_max_f32_e32 v18, 0, v2
	v_accvgpr_read_b32 v2, a14
	v_add_f32_e32 v2, v4, v2
	v_max_f32_e32 v19, 0, v2
	v_accvgpr_read_b32 v2, a15
	v_add_f32_e32 v2, v5, v2
	v_max_f32_e32 v20, 0, v2
	v_cvt_pk_f16_f32 v4, v9, v10
	v_cvt_pk_f16_f32 v3, v7, v8
	v_cvt_pk_f16_f32 v2, v1, v6
	ds_read_b128 v[6:9], v0 offset:51200
	v_cvt_pk_f16_f32 v5, v11, v12
	s_waitcnt lgkmcnt(0)
	s_nop 0
	v_mfma_f32_32x32x16_f16 a[32:47], v[6:9], v[2:5], a[32:47]
	ds_read_b128 v[6:9], v0 offset:52224
	v_cvt_pk_f16_f32 v5, v19, v20
	v_cvt_pk_f16_f32 v4, v17, v18
	v_cvt_pk_f16_f32 v3, v15, v16
	v_cvt_pk_f16_f32 v2, v13, v14
	s_waitcnt lgkmcnt(0)
	s_nop 0
	v_mfma_f32_32x32x16_f16 a[32:47], v[6:9], v[2:5], a[32:47]
	s_and_saveexec_b64 s[2:3], s[0:1]
	s_cbranch_execz .LBB3_39
	v_accvgpr_read_b32 v0, a80
	v_accvgpr_read_b32 v6, a86
	v_accvgpr_read_b32 v7, a87
	v_accvgpr_read_b32 v8, a88
	v_accvgpr_read_b32 v9, a89
	v_accvgpr_read_b32 v10, a90
	v_accvgpr_read_b32 v11, a91
	v_accvgpr_read_b32 v12, a92
	v_accvgpr_read_b32 v13, a93
	v_accvgpr_read_b32 v14, a94
	v_accvgpr_read_b32 v15, a95
	v_accvgpr_read_b32 v6, a32
	v_accvgpr_read_b32 v14, a40
	v_accvgpr_read_b32 v15, a41
	v_accvgpr_read_b32 v16, a42
	v_accvgpr_read_b32 v17, a43
	v_accvgpr_read_b32 v18, a44
	v_accvgpr_read_b32 v19, a45
	v_accvgpr_read_b32 v20, a46
	v_accvgpr_read_b32 v21, a47
	ds_read_b128 v[14:17], v22 offset:54016
	ds_read_b128 v[18:21], v22 offset:54080
	v_accvgpr_read_b32 v12, a38
	v_accvgpr_read_b32 v13, a39
	v_lshlrev_b32_e32 v24, 2, v85
	v_accvgpr_read_b32 v1, a81
	v_accvgpr_read_b32 v7, a33
	v_mad_i64_i32 v[12:13], s[0:1], v80, 40, s[18:19]
	v_ashrrev_i32_e32 v25, 31, v24
	v_accvgpr_read_b32 v3, a83
	v_accvgpr_read_b32 v9, a35
	v_lshl_add_u64 v[22:23], v[24:25], 2, v[12:13]
	v_mov_b32_e32 v25, v1
	s_waitcnt lgkmcnt(1)
	v_mov_b32_e32 v27, v15
	v_mov_b32_e32 v1, v7
	s_waitcnt lgkmcnt(0)
	v_mov_b32_e32 v15, v19
	v_accvgpr_read_b32 v2, a82
	v_accvgpr_read_b32 v8, a34
	v_pk_add_f32 v[0:1], v[0:1], v[14:15]
	v_mov_b32_e32 v7, v3
	v_mov_b32_e32 v15, v17
	v_mov_b32_e32 v3, v9
	v_mov_b32_e32 v17, v21
	v_mov_b32_e32 v24, v6
	v_mov_b32_e32 v26, v18
	v_mov_b32_e32 v6, v8
	v_mov_b32_e32 v14, v20
	v_pk_add_f32 v[2:3], v[2:3], v[16:17]
	v_pk_add_f32 v[24:25], v[24:25], v[26:27]
	s_waitcnt vmcnt(0)
	v_pk_mul_f32 v[0:1], v[82:83], v[0:1]
	v_pk_add_f32 v[6:7], v[6:7], v[14:15]
	v_pk_mul_f32 v[2:3], v[82:83], v[2:3]
	v_accvgpr_read_b32 v4, a84
	v_accvgpr_read_b32 v5, a85
	v_accvgpr_read_b32 v10, a36
	v_accvgpr_read_b32 v11, a37
	v_pk_fma_f32 v[0:1], v[82:83], v[24:25], v[0:1] op_sel:[1,0,0] op_sel_hi:[0,1,1]
	v_pk_fma_f32 v[2:3], v[82:83], v[6:7], v[2:3] op_sel:[1,0,0] op_sel_hi:[0,1,1]
	v_cmp_eq_u32_e32 vcc, 0, v85
	global_store_dwordx4 v[22:23], v[0:3], off
	s_and_b64 exec, exec, vcc
	s_cbranch_execz .LBB3_39
	s_mov_b32 s0, 0xd000
	v_add_u32_e64 v0, s0, 0
	ds_read2_b64 v[0:3], v0 offset0:100 offset1:108
	v_mov_b32_e32 v9, v5
	v_mov_b32_e32 v5, v11
	v_mov_b32_e32 v8, v10
	v_pk_mov_b32 v[6:7], v[82:83], v[82:83] op_sel:[1,0]
	s_waitcnt lgkmcnt(0)
	v_mov_b32_e32 v15, v1
	v_mov_b32_e32 v1, v3
	v_mov_b32_e32 v14, v2
	v_pk_add_f32 v[0:1], v[4:5], v[0:1]
	v_pk_add_f32 v[8:9], v[8:9], v[14:15]
	v_pk_mul_f32 v[0:1], v[82:83], v[0:1]
	s_nop 0
	v_pk_fma_f32 v[0:1], v[6:7], v[8:9], v[0:1]
	global_store_dwordx2 v[12:13], v[0:1], off offset:32
